# residual epilogues: row-sum shfl_xor 16/32 via permlane16/32 swap instead of ds_bpermute
# baseline (speedup 1.0000x reference)
; __device__ __forceinline__ u64_t* ssq_ptr(unsigned char* ws, int v) { return (u64_t*)(ws + CTL_SSQ) + (size_t)v * NTOK; }
; __device__ __forceinline__ u64_t ssq_fix(float ss) { return (u64_t)(ss * 16777216.0f); }
; #define ROW_FENCE() asm volatile("" ::: "memory")
; __device__ __forceinline__ u32x4 pack8(const f32x4& a, const f32x4& b) { u32x4 w; w.x = pk_bf16(a[0], a[1]); w.y = pk_bf16(a[2], a[3]); w.z = pk_bf16(b[0], b[1]); w.w = pk_bf16(b[2], b[3]); return w; }
;     __device__ __forceinline__ void operator()(const f32x4 (&acc)[2][2][4][2], const pg8::Unit& u, int wr, int wc, int fr, int fq) const {
;         bf16_t* xb = (bf16_t*)(ws + WS_XB); u64_t* ssq = ssq_ptr(ws, v);
;         float osc = 1.0f; if constexpr (SC) osc = __uint_as_float(((const unsigned*)(ws + CTL_AMAX))[AMAX_W2]) * (1.0f / 256.0f);
;         const int col = u.pn * 256 + wc * 32 + 8 * fq;
; #pragma unroll
;         for (int ai = 0; ai < 2; ++ai) {
;             u32x4 bs[4][2];
; #pragma unroll
;             for (int m = 0; m < 4; ++m) { const size_t off = (size_t)(u.pm * 256 + ai * 128 + wr * 64 + m * 16 + fr) * D + col;
; #pragma unroll
;                 for (int bj = 0; bj < 2; ++bj) bs[m][bj] = *(const u32x4*)(xb + off + bj * 128); }
;             ROW_FENCE();
; #pragma unroll
;             for (int m = 0; m < 4; ++m) {
;                 const int row = u.pm * 256 + ai * 128 + wr * 64 + m * 16 + fr; const size_t off = (size_t)row * D + col; float ss = 0.f;
;                 float rsc = osc; if constexpr (SC) asm volatile("" : "+v"(rsc));
; #pragma unroll
;                 for (int bj = 0; bj < 2; ++bj) { f32x4 b0, b1; unpack8(bs[m][bj], b0, b1); const f32x4 x0 = SC ? b0 + acc[ai][bj][m][0] * rsc : b0 + acc[ai][bj][m][0], x1 = SC ? b1 + acc[ai][bj][m][1] * rsc : b1 + acc[ai][bj][m][1];
;                     if (!dry) *(u32x4*)(xb + off + bj * 128) = pack8(x0, x1);
;                     ss += ((x0[0] * x0[0] + x0[1] * x0[1]) + (x0[2] * x0[2] + x0[3] * x0[3])) + ((x1[0] * x1[0] + x1[1] * x1[1]) + (x1[2] * x1[2] + x1[3] * x1[3])); }
;                 ss += __shfl_xor(ss, 16); ss += __shfl_xor(ss, 32);
;                 if (fq == 0 && !dry) atomicAdd(ssq + row, ssq_fix(ss));
;             }
.LBB0_1089:
	s_mov_b32 s11, s93
	v_and_b32_e32 v170, 64, v251
	v_mbcnt_lo_u32_b32 v130, -1, s11
	v_mbcnt_hi_u32_b32 v171, -1, v130
	s_lshl_b32 s11, s45, 8
	v_ashrrev_i32_e32 v130, 1, v171
	s_or_b32 s11, s11, s40
	v_and_b32_e32 v130, -8, v130
	v_add_u32_e32 v130, s11, v130
	s_lshl_b32 s11, s18, 8
	s_add_i32 s11, s11, s39
	v_and_or_b32 v156, v171, 15, s11
	v_ashrrev_i32_e32 v131, 31, v130
	v_ashrrev_i32_e32 v157, 31, v156
	v_lshl_add_u64 v[158:159], v[130:131], 1, s[6:7]
	v_lshlrev_b64 v[130:131], 11, v[156:157]
	v_lshl_add_u64 v[180:181], v[158:159], 0, v[130:131]
	flat_load_dwordx4 v[172:175], v[180:181]
	flat_load_dwordx4 v[176:179], v[180:181] offset:256
	v_or_b32_e32 v130, 16, v156
	v_or_b32_e32 v132, 32, v156
	v_or_b32_e32 v134, 48, v156
	v_ashrrev_i32_e32 v131, 31, v130
	v_ashrrev_i32_e32 v133, 31, v132
	v_ashrrev_i32_e32 v135, 31, v134
	v_lshlrev_b64 v[130:131], 11, v[130:131]
	v_lshlrev_b64 v[132:133], 11, v[132:133]
	v_lshlrev_b64 v[134:135], 11, v[134:135]
	v_lshl_add_u64 v[168:169], v[158:159], 0, v[130:131]
	v_lshl_add_u64 v[162:163], v[158:159], 0, v[132:133]
	v_lshl_add_u64 v[160:161], v[158:159], 0, v[134:135]
	flat_load_dwordx4 v[150:153], v[168:169]
	flat_load_dwordx4 v[146:149], v[168:169] offset:256
	flat_load_dwordx4 v[142:145], v[162:163]
	flat_load_dwordx4 v[138:141], v[162:163] offset:256
	flat_load_dwordx4 v[134:137], v[160:161]
	flat_load_dwordx4 v[130:133], v[160:161] offset:256
	v_xor_b32_e32 v167, 16, v251
	v_add_u32_e32 v170, 64, v170
	v_xor_b32_e32 v182, 32, v251
	v_cmp_lt_i32_e32 vcc, v167, v170
	s_waitcnt vmcnt(0) lgkmcnt(0)
	v_and_b32_e32 v183, 0xffff0000, v172
	v_cndmask_b32_e32 v167, v251, v167, vcc
	v_cmp_lt_i32_e32 vcc, v182, v170
	v_lshlrev_b32_e32 v170, 2, v167
	v_lshlrev_b32_e32 v184, 16, v174
	v_cndmask_b32_e32 v182, v251, v182, vcc
	v_lshlrev_b32_e32 v167, 2, v182
	v_lshlrev_b32_e32 v182, 16, v172
	v_lshlrev_b32_e32 v172, 16, v173
	v_and_b32_e32 v173, 0xffff0000, v173
	v_and_b32_e32 v185, 0xffff0000, v174
	v_lshlrev_b32_e32 v174, 16, v175
	v_and_b32_e32 v175, 0xffff0000, v175
	v_lshlrev_b32_e32 v186, 16, v176
	v_and_b32_e32 v187, 0xffff0000, v176
	v_lshlrev_b32_e32 v176, 16, v177
	v_and_b32_e32 v177, 0xffff0000, v177
	v_lshlrev_b32_e32 v188, 16, v178
	v_and_b32_e32 v189, 0xffff0000, v178
	v_lshlrev_b32_e32 v178, 16, v179
	v_and_b32_e32 v179, 0xffff0000, v179
	v_pk_add_f32 v[128:129], v[128:129], v[172:173]
	v_pk_add_f32 v[126:127], v[126:127], v[182:183]
	v_pk_add_f32 v[124:125], v[124:125], v[174:175]
	v_pk_add_f32 v[122:123], v[122:123], v[184:185]
	v_pk_add_f32 v[120:121], v[120:121], v[176:177]
	v_pk_add_f32 v[118:119], v[118:119], v[186:187]
	v_pk_add_f32 v[172:173], v[116:117], v[178:179]
	v_pk_add_f32 v[174:175], v[114:115], v[188:189]
	v_cmp_gt_u32_e32 vcc, 16, v171
	v_cvt_pk_bf16_f32 v114, v126, v127
	v_cvt_pk_bf16_f32 v115, v128, v129
	v_mul_f32_e32 v116, v127, v127
	v_mul_f32_e32 v117, v129, v129
	v_mul_f32_e32 v127, v123, v123
	v_mul_f32_e32 v129, v125, v125
	v_mul_f32_e32 v171, v119, v119
	v_mul_f32_e32 v176, v121, v121
	v_mul_f32_e32 v177, v175, v175
	v_mul_f32_e32 v178, v173, v173
	v_fmac_f32_e32 v116, v126, v126
	v_fmac_f32_e32 v117, v128, v128
	v_fmac_f32_e32 v127, v122, v122
	v_fmac_f32_e32 v129, v124, v124
	v_fmac_f32_e32 v171, v118, v118
	v_fmac_f32_e32 v176, v120, v120
	v_fmac_f32_e32 v177, v174, v174
	v_fmac_f32_e32 v178, v172, v172
	v_add_f32_e32 v116, v116, v117
	v_add_f32_e32 v117, v127, v129
	v_add_f32_e32 v126, v171, v176
	v_add_f32_e32 v127, v177, v178
	v_add_f32_e32 v116, v116, v117
	v_add_f32_e32 v117, v126, v127
	v_add_f32_e32 v126, v116, v117
	v_mov_b32_e32 v127, v126
	s_nop 1
	v_permlane16_swap_b32_e32 v126, v127
	v_cvt_pk_bf16_f32 v116, v122, v123
	v_cvt_pk_bf16_f32 v117, v124, v125
	flat_store_dwordx4 v[180:181], v[114:117]
	s_waitcnt lgkmcnt(0)
	s_nop 0
	v_add_f32_e32 v114, v126, v127
	v_mov_b32_e32 v115, v114
	s_nop 1
	v_permlane32_swap_b32_e32 v114, v115
	v_cvt_pk_bf16_f32 v116, v118, v119
	v_cvt_pk_bf16_f32 v117, v120, v121
	v_cvt_pk_bf16_f32 v118, v174, v175
	v_cvt_pk_bf16_f32 v119, v172, v173
	flat_store_dwordx4 v[180:181], v[116:119] offset:256
	s_and_saveexec_b64 s[18:19], vcc
	s_cbranch_execz .LBB0_1091
	s_waitcnt lgkmcnt(0)
	v_add_f32_e32 v114, v114, v115
	v_mul_f32_e32 v114, 0x4b800000, v114
	v_trunc_f32_e32 v114, v114
	v_mul_f32_e32 v115, 0x2f800000, v114
	v_floor_f32_e32 v115, v115
	v_fmac_f32_e32 v114, 0xcf800000, v115
	v_cvt_u32_f32_e32 v114, v114
	v_cvt_u32_f32_e32 v115, v115
	v_lshl_add_u64 v[116:117], v[156:157], 3, s[8:9]
	flat_atomic_add_x2 v[116:117], v[114:115]
; __device__ __forceinline__ u64_t ssq_fix(float ss) { return (u64_t)(ss * 16777216.0f); }
; __device__ __forceinline__ u32x4 pack8(const f32x4& a, const f32x4& b) { u32x4 w; w.x = pk_bf16(a[0], a[1]); w.y = pk_bf16(a[2], a[3]); w.z = pk_bf16(b[0], b[1]); w.w = pk_bf16(b[2], b[3]); return w; }
; __device__ __forceinline__ void unpack8(const u32x4& w, f32x4& a, f32x4& b) { a = (f32x4){bf_lo(w.x), bf_hi(w.x), bf_lo(w.y), bf_hi(w.y)}; b = (f32x4){bf_lo(w.z), bf_hi(w.z), bf_lo(w.w), bf_hi(w.w)}; }
;     __device__ __forceinline__ void operator()(const f32x4 (&acc)[2][2][4][2], const pg8::Unit& u, int wr, int wc, int fr, int fq) const {
;     ...
; #pragma unroll
;             for (int m = 0; m < 4; ++m) {
;                 const int row = u.pm * 256 + ai * 128 + wr * 64 + m * 16 + fr; const size_t off = (size_t)row * D + col; float ss = 0.f;
;                 float rsc = osc; if constexpr (SC) asm volatile("" : "+v"(rsc));
; #pragma unroll
;                 for (int bj = 0; bj < 2; ++bj) { f32x4 b0, b1; unpack8(bs[m][bj], b0, b1); const f32x4 x0 = SC ? b0 + acc[ai][bj][m][0] * rsc : b0 + acc[ai][bj][m][0], x1 = SC ? b1 + acc[ai][bj][m][1] * rsc : b1 + acc[ai][bj][m][1];
;                     if (!dry) *(u32x4*)(xb + off + bj * 128) = pack8(x0, x1);
;                     ss += ((x0[0] * x0[0] + x0[1] * x0[1]) + (x0[2] * x0[2] + x0[3] * x0[3])) + ((x1[0] * x1[0] + x1[1] * x1[1]) + (x1[2] * x1[2] + x1[3] * x1[3])); }
;                 ss += __shfl_xor(ss, 16); ss += __shfl_xor(ss, 32);
;                 if (fq == 0 && !dry) atomicAdd(ssq + row, ssq_fix(ss));
;             }
.LBB0_1091:
	s_or_b64 exec, exec, s[18:19]
	v_lshlrev_b32_e32 v114, 16, v150
	s_waitcnt lgkmcnt(0)
	v_and_b32_e32 v115, 0xffff0000, v150
	v_lshlrev_b32_e32 v116, 16, v151
	v_and_b32_e32 v117, 0xffff0000, v151
	v_lshlrev_b32_e32 v118, 16, v152
	v_and_b32_e32 v119, 0xffff0000, v152
	v_lshlrev_b32_e32 v120, 16, v153
	v_and_b32_e32 v121, 0xffff0000, v153
	v_pk_add_f32 v[108:109], v[108:109], v[114:115]
	v_pk_add_f32 v[110:111], v[110:111], v[116:117]
	v_pk_add_f32 v[114:115], v[106:107], v[120:121]
	v_pk_add_f32 v[106:107], v[104:105], v[118:119]
	v_cvt_pk_bf16_f32 v104, v108, v109
	v_mul_f32_e32 v109, v109, v109
	v_fmac_f32_e32 v109, v108, v108
	v_mul_f32_e32 v108, v111, v111
	v_fmac_f32_e32 v108, v110, v110
	v_cvt_pk_bf16_f32 v105, v110, v111
	v_add_f32_e32 v108, v109, v108
	v_mul_f32_e32 v109, v107, v107
	v_mul_f32_e32 v110, v115, v115
	v_fmac_f32_e32 v109, v106, v106
	v_fmac_f32_e32 v110, v114, v114
	v_add_f32_e32 v109, v109, v110
	v_add_f32_e32 v120, v108, v109
	v_lshlrev_b32_e32 v108, 16, v146
	v_and_b32_e32 v109, 0xffff0000, v146
	v_lshlrev_b32_e32 v110, 16, v147
	v_and_b32_e32 v111, 0xffff0000, v147
	v_lshlrev_b32_e32 v116, 16, v148
	v_and_b32_e32 v117, 0xffff0000, v148
	v_pk_add_f32 v[102:103], v[102:103], v[110:111]
	v_pk_add_f32 v[100:101], v[100:101], v[108:109]
	v_lshlrev_b32_e32 v118, 16, v149
	v_and_b32_e32 v119, 0xffff0000, v149
	v_pk_add_f32 v[110:111], v[96:97], v[116:117]
	v_mul_f32_e32 v96, v101, v101
	v_mul_f32_e32 v97, v103, v103
	v_pk_add_f32 v[108:109], v[98:99], v[118:119]
	v_fmac_f32_e32 v96, v100, v100
	v_fmac_f32_e32 v97, v102, v102
	v_add_f32_e32 v96, v96, v97
	v_mul_f32_e32 v97, v111, v111
	v_mul_f32_e32 v98, v109, v109
	v_fmac_f32_e32 v97, v110, v110
	v_fmac_f32_e32 v98, v108, v108
	v_add_f32_e32 v97, v97, v98
	v_add_f32_e32 v96, v96, v97
	v_add_f32_e32 v96, v120, v96
	v_mov_b32_e32 v97, v96
	s_nop 1
	v_permlane16_swap_b32_e32 v96, v97
	v_cvt_pk_bf16_f32 v106, v106, v107
	v_cvt_pk_bf16_f32 v107, v114, v115
	v_cvt_pk_bf16_f32 v98, v100, v101
	v_cvt_pk_bf16_f32 v99, v102, v103
	s_waitcnt lgkmcnt(0)
	v_add_f32_e32 v96, v96, v97
	v_mov_b32_e32 v97, v96
	s_nop 1
	v_permlane32_swap_b32_e32 v96, v97
	v_cvt_pk_bf16_f32 v100, v110, v111
	v_cvt_pk_bf16_f32 v101, v108, v109
	flat_store_dwordx4 v[168:169], v[104:107]
	flat_store_dwordx4 v[168:169], v[98:101] offset:256
	s_and_saveexec_b64 s[18:19], vcc
	s_cbranch_execz .LBB0_1093
	s_waitcnt lgkmcnt(0)
	v_add_f32_e32 v96, v96, v97
	v_mul_f32_e32 v96, 0x4b800000, v96
	v_trunc_f32_e32 v96, v96
	v_mul_f32_e32 v97, 0x2f800000, v96
	v_floor_f32_e32 v97, v97
	v_fmac_f32_e32 v96, 0xcf800000, v97
	v_cvt_u32_f32_e32 v96, v96
	v_cvt_u32_f32_e32 v97, v97
	v_lshl_add_u64 v[98:99], v[156:157], 3, s[8:9]
	flat_atomic_add_x2 v[98:99], v[96:97] offset:128
.LBB0_1093:
	s_or_b64 exec, exec, s[18:19]
	v_lshlrev_b32_e32 v96, 16, v142
	s_waitcnt lgkmcnt(0)
	v_and_b32_e32 v97, 0xffff0000, v142
	v_lshlrev_b32_e32 v98, 16, v143
	v_and_b32_e32 v99, 0xffff0000, v143
	v_lshlrev_b32_e32 v100, 16, v144
	v_and_b32_e32 v101, 0xffff0000, v144
	v_lshlrev_b32_e32 v102, 16, v145
	v_and_b32_e32 v103, 0xffff0000, v145
	v_pk_add_f32 v[92:93], v[92:93], v[96:97]
	v_pk_add_f32 v[94:95], v[94:95], v[98:99]
	v_pk_add_f32 v[96:97], v[90:91], v[102:103]
	v_pk_add_f32 v[90:91], v[88:89], v[100:101]
	v_cvt_pk_bf16_f32 v88, v92, v93
	v_mul_f32_e32 v93, v93, v93
	v_fmac_f32_e32 v93, v92, v92
	v_mul_f32_e32 v92, v95, v95
	v_fmac_f32_e32 v92, v94, v94
	v_cvt_pk_bf16_f32 v89, v94, v95
	v_add_f32_e32 v92, v93, v92
	v_mul_f32_e32 v93, v91, v91
	v_mul_f32_e32 v94, v97, v97
	v_fmac_f32_e32 v93, v90, v90
	v_fmac_f32_e32 v94, v96, v96
	v_add_f32_e32 v93, v93, v94
	v_add_f32_e32 v102, v92, v93
	v_lshlrev_b32_e32 v92, 16, v138
	v_and_b32_e32 v93, 0xffff0000, v138
	v_lshlrev_b32_e32 v94, 16, v139
	v_and_b32_e32 v95, 0xffff0000, v139
	v_lshlrev_b32_e32 v98, 16, v140
	v_and_b32_e32 v99, 0xffff0000, v140
	v_pk_add_f32 v[86:87], v[86:87], v[94:95]
	v_pk_add_f32 v[84:85], v[84:85], v[92:93]
	v_lshlrev_b32_e32 v100, 16, v141
	v_and_b32_e32 v101, 0xffff0000, v141
	v_pk_add_f32 v[94:95], v[80:81], v[98:99]
	v_mul_f32_e32 v80, v85, v85
	v_mul_f32_e32 v81, v87, v87
	v_pk_add_f32 v[92:93], v[82:83], v[100:101]
	v_fmac_f32_e32 v80, v84, v84
	v_fmac_f32_e32 v81, v86, v86
	v_add_f32_e32 v80, v80, v81
	v_mul_f32_e32 v81, v95, v95
	v_mul_f32_e32 v82, v93, v93
	v_fmac_f32_e32 v81, v94, v94
	v_fmac_f32_e32 v82, v92, v92
	v_add_f32_e32 v81, v81, v82
	v_add_f32_e32 v80, v80, v81
	v_add_f32_e32 v80, v102, v80
	v_mov_b32_e32 v81, v80
	s_nop 1
	v_permlane16_swap_b32_e32 v80, v81
	v_cvt_pk_bf16_f32 v90, v90, v91
	v_cvt_pk_bf16_f32 v91, v96, v97
	v_cvt_pk_bf16_f32 v82, v84, v85
	v_cvt_pk_bf16_f32 v83, v86, v87
	s_waitcnt lgkmcnt(0)
	v_add_f32_e32 v80, v80, v81
	v_mov_b32_e32 v81, v80
	s_nop 1
	v_permlane32_swap_b32_e32 v80, v81
	v_cvt_pk_bf16_f32 v84, v94, v95
	v_cvt_pk_bf16_f32 v85, v92, v93
	flat_store_dwordx4 v[162:163], v[88:91]
	flat_store_dwordx4 v[162:163], v[82:85] offset:256
	s_and_saveexec_b64 s[18:19], vcc
	s_cbranch_execz .LBB0_1095
	s_waitcnt lgkmcnt(0)
	v_add_f32_e32 v80, v80, v81
	v_mul_f32_e32 v80, 0x4b800000, v80
	v_trunc_f32_e32 v80, v80
	v_mul_f32_e32 v81, 0x2f800000, v80
	v_floor_f32_e32 v81, v81
	v_fmac_f32_e32 v80, 0xcf800000, v81
	v_cvt_u32_f32_e32 v80, v80
	v_cvt_u32_f32_e32 v81, v81
	v_lshl_add_u64 v[82:83], v[156:157], 3, s[8:9]
	flat_atomic_add_x2 v[82:83], v[80:81] offset:256
; __device__ __forceinline__ u64_t ssq_fix(float ss) { return (u64_t)(ss * 16777216.0f); }
; __device__ __forceinline__ u32x4 pack8(const f32x4& a, const f32x4& b) { u32x4 w; w.x = pk_bf16(a[0], a[1]); w.y = pk_bf16(a[2], a[3]); w.z = pk_bf16(b[0], b[1]); w.w = pk_bf16(b[2], b[3]); return w; }
; __device__ __forceinline__ void unpack8(const u32x4& w, f32x4& a, f32x4& b) { a = (f32x4){bf_lo(w.x), bf_hi(w.x), bf_lo(w.y), bf_hi(w.y)}; b = (f32x4){bf_lo(w.z), bf_hi(w.z), bf_lo(w.w), bf_hi(w.w)}; }
;     __device__ __forceinline__ void operator()(const f32x4 (&acc)[2][2][4][2], const pg8::Unit& u, int wr, int wc, int fr, int fq) const {
;     ...
; #pragma unroll
;             for (int m = 0; m < 4; ++m) {
;                 const int row = u.pm * 256 + ai * 128 + wr * 64 + m * 16 + fr; const size_t off = (size_t)row * D + col; float ss = 0.f;
;                 float rsc = osc; if constexpr (SC) asm volatile("" : "+v"(rsc));
; #pragma unroll
;                 for (int bj = 0; bj < 2; ++bj) { f32x4 b0, b1; unpack8(bs[m][bj], b0, b1); const f32x4 x0 = SC ? b0 + acc[ai][bj][m][0] * rsc : b0 + acc[ai][bj][m][0], x1 = SC ? b1 + acc[ai][bj][m][1] * rsc : b1 + acc[ai][bj][m][1];
;                     if (!dry) *(u32x4*)(xb + off + bj * 128) = pack8(x0, x1);
;                     ss += ((x0[0] * x0[0] + x0[1] * x0[1]) + (x0[2] * x0[2] + x0[3] * x0[3])) + ((x1[0] * x1[0] + x1[1] * x1[1]) + (x1[2] * x1[2] + x1[3] * x1[3])); }
;                 ss += __shfl_xor(ss, 16); ss += __shfl_xor(ss, 32);
;                 if (fq == 0 && !dry) atomicAdd(ssq + row, ssq_fix(ss));
;             }
.LBB0_1095:
	s_or_b64 exec, exec, s[18:19]
	v_lshlrev_b32_e32 v80, 16, v134
	s_waitcnt lgkmcnt(0)
	v_and_b32_e32 v81, 0xffff0000, v134
	v_lshlrev_b32_e32 v82, 16, v135
	v_and_b32_e32 v83, 0xffff0000, v135
	v_lshlrev_b32_e32 v84, 16, v136
	v_and_b32_e32 v85, 0xffff0000, v136
	v_lshlrev_b32_e32 v86, 16, v137
	v_and_b32_e32 v87, 0xffff0000, v137
	v_pk_add_f32 v[76:77], v[76:77], v[80:81]
	v_pk_add_f32 v[78:79], v[78:79], v[82:83]
	v_pk_add_f32 v[80:81], v[74:75], v[86:87]
	v_pk_add_f32 v[74:75], v[72:73], v[84:85]
	v_cvt_pk_bf16_f32 v72, v76, v77
	v_mul_f32_e32 v77, v77, v77
	v_fmac_f32_e32 v77, v76, v76
	v_mul_f32_e32 v76, v79, v79
	v_fmac_f32_e32 v76, v78, v78
	v_cvt_pk_bf16_f32 v73, v78, v79
	v_add_f32_e32 v76, v77, v76
	v_mul_f32_e32 v77, v75, v75
	v_mul_f32_e32 v78, v81, v81
	v_fmac_f32_e32 v77, v74, v74
	v_fmac_f32_e32 v78, v80, v80
	v_add_f32_e32 v77, v77, v78
	v_add_f32_e32 v86, v76, v77
	v_lshlrev_b32_e32 v76, 16, v130
	v_and_b32_e32 v77, 0xffff0000, v130
	v_lshlrev_b32_e32 v78, 16, v131
	v_and_b32_e32 v79, 0xffff0000, v131
	v_lshlrev_b32_e32 v82, 16, v132
	v_and_b32_e32 v83, 0xffff0000, v132
	v_pk_add_f32 v[70:71], v[70:71], v[78:79]
	v_pk_add_f32 v[68:69], v[68:69], v[76:77]
	v_lshlrev_b32_e32 v84, 16, v133
	v_and_b32_e32 v85, 0xffff0000, v133
	v_pk_add_f32 v[78:79], v[64:65], v[82:83]
	v_mul_f32_e32 v64, v69, v69
	v_mul_f32_e32 v65, v71, v71
	v_pk_add_f32 v[76:77], v[66:67], v[84:85]
	v_fmac_f32_e32 v64, v68, v68
	v_fmac_f32_e32 v65, v70, v70
	v_add_f32_e32 v64, v64, v65
	v_mul_f32_e32 v65, v79, v79
	v_mul_f32_e32 v66, v77, v77
	v_fmac_f32_e32 v65, v78, v78
	v_fmac_f32_e32 v66, v76, v76
	v_add_f32_e32 v65, v65, v66
	v_add_f32_e32 v64, v64, v65
	v_add_f32_e32 v64, v86, v64
	v_mov_b32_e32 v65, v64
	s_nop 1
	v_permlane16_swap_b32_e32 v64, v65
	v_cvt_pk_bf16_f32 v74, v74, v75
	v_cvt_pk_bf16_f32 v75, v80, v81
	v_cvt_pk_bf16_f32 v66, v68, v69
	v_cvt_pk_bf16_f32 v67, v70, v71
	s_waitcnt lgkmcnt(0)
	v_add_f32_e32 v64, v64, v65
	v_mov_b32_e32 v65, v64
	s_nop 1
	v_permlane32_swap_b32_e32 v64, v65
	v_cvt_pk_bf16_f32 v68, v78, v79
	v_cvt_pk_bf16_f32 v69, v76, v77
	flat_store_dwordx4 v[160:161], v[72:75]
	flat_store_dwordx4 v[160:161], v[66:69] offset:256
	s_and_saveexec_b64 s[18:19], vcc
	s_cbranch_execz .LBB0_1097
	s_waitcnt lgkmcnt(0)
	v_add_f32_e32 v64, v64, v65
	v_mul_f32_e32 v64, 0x4b800000, v64
	v_trunc_f32_e32 v64, v64
	v_mul_f32_e32 v65, 0x2f800000, v64
	v_floor_f32_e32 v65, v65
	v_fmac_f32_e32 v64, 0xcf800000, v65
	v_cvt_u32_f32_e32 v64, v64
	v_cvt_u32_f32_e32 v65, v65
	v_lshl_add_u64 v[66:67], v[156:157], 3, s[8:9]
	flat_atomic_add_x2 v[66:67], v[64:65] offset:384
.LBB0_1097:
	s_or_b64 exec, exec, s[18:19]
	v_add_u32_e32 v64, 0x80, v156
	s_waitcnt lgkmcnt(0)
	v_ashrrev_i32_e32 v65, 31, v64
	v_lshlrev_b64 v[64:65], 11, v[64:65]
	v_lshl_add_u64 v[94:95], v[158:159], 0, v[64:65]
	flat_load_dwordx4 v[96:99], v[94:95]
	flat_load_dwordx4 v[100:103], v[94:95] offset:256
	v_add_u32_e32 v64, 0x90, v156
	v_ashrrev_i32_e32 v65, 31, v64
	v_lshlrev_b64 v[64:65], 11, v[64:65]
	v_lshl_add_u64 v[92:93], v[158:159], 0, v[64:65]
	v_add_u32_e32 v64, 0xa0, v156
	v_ashrrev_i32_e32 v65, 31, v64
	v_lshlrev_b64 v[64:65], 11, v[64:65]
	v_lshl_add_u64 v[90:91], v[158:159], 0, v[64:65]
	v_add_u32_e32 v64, 0xb0, v156
	v_ashrrev_i32_e32 v65, 31, v64
	v_lshlrev_b64 v[64:65], 11, v[64:65]
	v_lshl_add_u64 v[88:89], v[158:159], 0, v[64:65]
	flat_load_dwordx4 v[84:87], v[92:93]
	flat_load_dwordx4 v[80:83], v[92:93] offset:256
	flat_load_dwordx4 v[76:79], v[90:91]
	flat_load_dwordx4 v[72:75], v[90:91] offset:256
	flat_load_dwordx4 v[68:71], v[88:89]
	flat_load_dwordx4 v[64:67], v[88:89] offset:256
	s_waitcnt vmcnt(0) lgkmcnt(0)
	v_lshlrev_b32_e32 v104, 16, v96
	v_and_b32_e32 v105, 0xffff0000, v96
	v_lshlrev_b32_e32 v96, 16, v97
	v_and_b32_e32 v97, 0xffff0000, v97
	v_lshlrev_b32_e32 v106, 16, v98
	v_and_b32_e32 v107, 0xffff0000, v98
	v_lshlrev_b32_e32 v98, 16, v99
	v_and_b32_e32 v99, 0xffff0000, v99
	v_pk_add_f32 v[62:63], v[62:63], v[96:97]
	v_pk_add_f32 v[60:61], v[60:61], v[104:105]
	v_pk_add_f32 v[96:97], v[58:59], v[98:99]
	v_pk_add_f32 v[98:99], v[56:57], v[106:107]
	v_cvt_pk_bf16_f32 v56, v60, v61
	v_cvt_pk_bf16_f32 v57, v62, v63
	v_cvt_pk_bf16_f32 v58, v98, v99
	v_cvt_pk_bf16_f32 v59, v96, v97
	flat_store_dwordx4 v[94:95], v[56:59]
	s_nop 1
	v_mul_f32_e32 v56, v61, v61
	v_mul_f32_e32 v57, v63, v63
	v_fmac_f32_e32 v56, v60, v60
	v_fmac_f32_e32 v57, v62, v62
	v_add_f32_e32 v56, v56, v57
	v_mul_f32_e32 v57, v99, v99
	v_mul_f32_e32 v58, v97, v97
	v_fmac_f32_e32 v57, v98, v98
	v_fmac_f32_e32 v58, v96, v96
	v_add_f32_e32 v57, v57, v58
	v_add_f32_e32 v96, v56, v57
	v_lshlrev_b32_e32 v56, 16, v100
	v_and_b32_e32 v57, 0xffff0000, v100
	v_lshlrev_b32_e32 v58, 16, v101
	v_and_b32_e32 v59, 0xffff0000, v101
	v_lshlrev_b32_e32 v60, 16, v102
	v_and_b32_e32 v61, 0xffff0000, v102
	v_lshlrev_b32_e32 v62, 16, v103
	v_and_b32_e32 v63, 0xffff0000, v103
	v_pk_add_f32 v[54:55], v[54:55], v[58:59]
	v_pk_add_f32 v[52:53], v[52:53], v[56:57]
	v_pk_add_f32 v[56:57], v[50:51], v[62:63]
	v_pk_add_f32 v[58:59], v[48:49], v[60:61]
	v_cvt_pk_bf16_f32 v48, v52, v53
	v_cvt_pk_bf16_f32 v49, v54, v55
	v_cvt_pk_bf16_f32 v50, v58, v59
	v_cvt_pk_bf16_f32 v51, v56, v57
	flat_store_dwordx4 v[94:95], v[48:51] offset:256
	s_nop 1
	v_mul_f32_e32 v48, v53, v53
	v_mul_f32_e32 v49, v55, v55
	v_fmac_f32_e32 v48, v52, v52
	v_fmac_f32_e32 v49, v54, v54
	v_add_f32_e32 v48, v48, v49
	v_mul_f32_e32 v49, v59, v59
	v_mul_f32_e32 v50, v57, v57
	v_fmac_f32_e32 v49, v58, v58
	v_fmac_f32_e32 v50, v56, v56
	v_add_f32_e32 v49, v49, v50
	v_add_f32_e32 v48, v48, v49
	v_add_f32_e32 v48, v96, v48
	v_mov_b32_e32 v49, v48
	s_nop 1
	v_permlane16_swap_b32_e32 v48, v49
	s_waitcnt lgkmcnt(0)
	v_add_f32_e32 v48, v48, v49
	v_mov_b32_e32 v49, v48
	s_nop 1
	v_permlane32_swap_b32_e32 v48, v49
	s_and_saveexec_b64 s[18:19], vcc
	s_cbranch_execz .LBB0_1099
	s_waitcnt lgkmcnt(0)
	v_add_f32_e32 v48, v48, v49
	v_mul_f32_e32 v48, 0x4b800000, v48
	v_trunc_f32_e32 v48, v48
	v_mul_f32_e32 v49, 0x2f800000, v48
	v_floor_f32_e32 v49, v49
	v_fmac_f32_e32 v48, 0xcf800000, v49
	v_cvt_u32_f32_e32 v48, v48
	v_cvt_u32_f32_e32 v49, v49
	v_lshl_add_u64 v[50:51], v[156:157], 3, s[8:9]
	flat_atomic_add_x2 v[50:51], v[48:49] offset:1024
; __device__ __forceinline__ u64_t ssq_fix(float ss) { return (u64_t)(ss * 16777216.0f); }
; __device__ __forceinline__ u32x4 pack8(const f32x4& a, const f32x4& b) { u32x4 w; w.x = pk_bf16(a[0], a[1]); w.y = pk_bf16(a[2], a[3]); w.z = pk_bf16(b[0], b[1]); w.w = pk_bf16(b[2], b[3]); return w; }
; __device__ __forceinline__ void unpack8(const u32x4& w, f32x4& a, f32x4& b) { a = (f32x4){bf_lo(w.x), bf_hi(w.x), bf_lo(w.y), bf_hi(w.y)}; b = (f32x4){bf_lo(w.z), bf_hi(w.z), bf_lo(w.w), bf_hi(w.w)}; }
;     __device__ __forceinline__ void operator()(const f32x4 (&acc)[2][2][4][2], const pg8::Unit& u, int wr, int wc, int fr, int fq) const {
;     ...
; #pragma unroll
;             for (int m = 0; m < 4; ++m) {
;                 const int row = u.pm * 256 + ai * 128 + wr * 64 + m * 16 + fr; const size_t off = (size_t)row * D + col; float ss = 0.f;
;                 float rsc = osc; if constexpr (SC) asm volatile("" : "+v"(rsc));
; #pragma unroll
;                 for (int bj = 0; bj < 2; ++bj) { f32x4 b0, b1; unpack8(bs[m][bj], b0, b1); const f32x4 x0 = SC ? b0 + acc[ai][bj][m][0] * rsc : b0 + acc[ai][bj][m][0], x1 = SC ? b1 + acc[ai][bj][m][1] * rsc : b1 + acc[ai][bj][m][1];
;                     if (!dry) *(u32x4*)(xb + off + bj * 128) = pack8(x0, x1);
;                     ss += ((x0[0] * x0[0] + x0[1] * x0[1]) + (x0[2] * x0[2] + x0[3] * x0[3])) + ((x1[0] * x1[0] + x1[1] * x1[1]) + (x1[2] * x1[2] + x1[3] * x1[3])); }
;                 ss += __shfl_xor(ss, 16); ss += __shfl_xor(ss, 32);
;                 if (fq == 0 && !dry) atomicAdd(ssq + row, ssq_fix(ss));
;             }
.LBB0_1099:
	s_or_b64 exec, exec, s[18:19]
	v_lshlrev_b32_e32 v48, 16, v84
	s_waitcnt lgkmcnt(0)
	v_and_b32_e32 v49, 0xffff0000, v84
	v_lshlrev_b32_e32 v50, 16, v85
	v_and_b32_e32 v51, 0xffff0000, v85
	v_lshlrev_b32_e32 v52, 16, v86
	v_and_b32_e32 v53, 0xffff0000, v86
	v_lshlrev_b32_e32 v54, 16, v87
	v_and_b32_e32 v55, 0xffff0000, v87
	v_pk_add_f32 v[44:45], v[44:45], v[48:49]
	v_pk_add_f32 v[46:47], v[46:47], v[50:51]
	v_pk_add_f32 v[48:49], v[42:43], v[54:55]
	v_pk_add_f32 v[42:43], v[40:41], v[52:53]
	v_cvt_pk_bf16_f32 v40, v44, v45
	v_mul_f32_e32 v45, v45, v45
	v_fmac_f32_e32 v45, v44, v44
	v_mul_f32_e32 v44, v47, v47
	v_fmac_f32_e32 v44, v46, v46
	v_cvt_pk_bf16_f32 v41, v46, v47
	v_add_f32_e32 v44, v45, v44
	v_mul_f32_e32 v45, v43, v43
	v_mul_f32_e32 v46, v49, v49
	v_fmac_f32_e32 v45, v42, v42
	v_fmac_f32_e32 v46, v48, v48
	v_add_f32_e32 v45, v45, v46
	v_add_f32_e32 v54, v44, v45
	v_lshlrev_b32_e32 v44, 16, v80
	v_and_b32_e32 v45, 0xffff0000, v80
	v_lshlrev_b32_e32 v46, 16, v81
	v_and_b32_e32 v47, 0xffff0000, v81
	v_lshlrev_b32_e32 v50, 16, v82
	v_and_b32_e32 v51, 0xffff0000, v82
	v_pk_add_f32 v[38:39], v[38:39], v[46:47]
	v_pk_add_f32 v[36:37], v[36:37], v[44:45]
	v_lshlrev_b32_e32 v52, 16, v83
	v_and_b32_e32 v53, 0xffff0000, v83
	v_pk_add_f32 v[46:47], v[32:33], v[50:51]
	v_mul_f32_e32 v32, v37, v37
	v_mul_f32_e32 v33, v39, v39
	v_pk_add_f32 v[44:45], v[34:35], v[52:53]
	v_fmac_f32_e32 v32, v36, v36
	v_fmac_f32_e32 v33, v38, v38
	v_add_f32_e32 v32, v32, v33
	v_mul_f32_e32 v33, v47, v47
	v_mul_f32_e32 v34, v45, v45
	v_fmac_f32_e32 v33, v46, v46
	v_fmac_f32_e32 v34, v44, v44
	v_add_f32_e32 v33, v33, v34
	v_add_f32_e32 v32, v32, v33
	v_add_f32_e32 v32, v54, v32
	v_mov_b32_e32 v33, v32
	s_nop 1
	v_permlane16_swap_b32_e32 v32, v33
	v_cvt_pk_bf16_f32 v42, v42, v43
	v_cvt_pk_bf16_f32 v43, v48, v49
	v_cvt_pk_bf16_f32 v34, v36, v37
	v_cvt_pk_bf16_f32 v35, v38, v39
	s_waitcnt lgkmcnt(0)
	v_add_f32_e32 v32, v32, v33
	v_mov_b32_e32 v33, v32
	s_nop 1
	v_permlane32_swap_b32_e32 v32, v33
	v_cvt_pk_bf16_f32 v36, v46, v47
	v_cvt_pk_bf16_f32 v37, v44, v45
	flat_store_dwordx4 v[92:93], v[40:43]
	flat_store_dwordx4 v[92:93], v[34:37] offset:256
	s_and_saveexec_b64 s[18:19], vcc
	s_cbranch_execz .LBB0_1101
	s_waitcnt lgkmcnt(0)
	v_add_f32_e32 v32, v32, v33
	v_mul_f32_e32 v32, 0x4b800000, v32
	v_trunc_f32_e32 v32, v32
	v_mul_f32_e32 v33, 0x2f800000, v32
	v_floor_f32_e32 v33, v33
	v_fmac_f32_e32 v32, 0xcf800000, v33
	v_cvt_u32_f32_e32 v32, v32
	v_cvt_u32_f32_e32 v33, v33
	v_lshl_add_u64 v[34:35], v[156:157], 3, s[8:9]
	flat_atomic_add_x2 v[34:35], v[32:33] offset:1152
; __device__ __forceinline__ u64_t ssq_fix(float ss) { return (u64_t)(ss * 16777216.0f); }
; __device__ __forceinline__ u32x4 pack8(const f32x4& a, const f32x4& b) { u32x4 w; w.x = pk_bf16(a[0], a[1]); w.y = pk_bf16(a[2], a[3]); w.z = pk_bf16(b[0], b[1]); w.w = pk_bf16(b[2], b[3]); return w; }
; __device__ __forceinline__ void unpack8(const u32x4& w, f32x4& a, f32x4& b) { a = (f32x4){bf_lo(w.x), bf_hi(w.x), bf_lo(w.y), bf_hi(w.y)}; b = (f32x4){bf_lo(w.z), bf_hi(w.z), bf_lo(w.w), bf_hi(w.w)}; }
;     __device__ __forceinline__ void operator()(const f32x4 (&acc)[2][2][4][2], const pg8::Unit& u, int wr, int wc, int fr, int fq) const {
;     ...
; #pragma unroll
;             for (int m = 0; m < 4; ++m) {
;                 const int row = u.pm * 256 + ai * 128 + wr * 64 + m * 16 + fr; const size_t off = (size_t)row * D + col; float ss = 0.f;
;                 float rsc = osc; if constexpr (SC) asm volatile("" : "+v"(rsc));
; #pragma unroll
;                 for (int bj = 0; bj < 2; ++bj) { f32x4 b0, b1; unpack8(bs[m][bj], b0, b1); const f32x4 x0 = SC ? b0 + acc[ai][bj][m][0] * rsc : b0 + acc[ai][bj][m][0], x1 = SC ? b1 + acc[ai][bj][m][1] * rsc : b1 + acc[ai][bj][m][1];
;                     if (!dry) *(u32x4*)(xb + off + bj * 128) = pack8(x0, x1);
;                     ss += ((x0[0] * x0[0] + x0[1] * x0[1]) + (x0[2] * x0[2] + x0[3] * x0[3])) + ((x1[0] * x1[0] + x1[1] * x1[1]) + (x1[2] * x1[2] + x1[3] * x1[3])); }
;                 ss += __shfl_xor(ss, 16); ss += __shfl_xor(ss, 32);
;                 if (fq == 0 && !dry) atomicAdd(ssq + row, ssq_fix(ss));
;             }
.LBB0_1101:
	s_or_b64 exec, exec, s[18:19]
	v_lshlrev_b32_e32 v32, 16, v76
	s_waitcnt lgkmcnt(0)
	v_and_b32_e32 v33, 0xffff0000, v76
	v_lshlrev_b32_e32 v34, 16, v77
	v_and_b32_e32 v35, 0xffff0000, v77
	v_lshlrev_b32_e32 v36, 16, v78
	v_and_b32_e32 v37, 0xffff0000, v78
	v_lshlrev_b32_e32 v38, 16, v79
	v_and_b32_e32 v39, 0xffff0000, v79
	v_pk_add_f32 v[28:29], v[28:29], v[32:33]
	v_pk_add_f32 v[30:31], v[30:31], v[34:35]
	v_pk_add_f32 v[32:33], v[26:27], v[38:39]
	v_pk_add_f32 v[26:27], v[24:25], v[36:37]
	v_cvt_pk_bf16_f32 v24, v28, v29
	v_mul_f32_e32 v29, v29, v29
	v_fmac_f32_e32 v29, v28, v28
	v_mul_f32_e32 v28, v31, v31
	v_fmac_f32_e32 v28, v30, v30
	v_cvt_pk_bf16_f32 v25, v30, v31
	v_add_f32_e32 v28, v29, v28
	v_mul_f32_e32 v29, v27, v27
	v_mul_f32_e32 v30, v33, v33
	v_fmac_f32_e32 v29, v26, v26
	v_fmac_f32_e32 v30, v32, v32
	v_add_f32_e32 v29, v29, v30
	v_add_f32_e32 v38, v28, v29
	v_lshlrev_b32_e32 v28, 16, v72
	v_and_b32_e32 v29, 0xffff0000, v72
	v_lshlrev_b32_e32 v30, 16, v73
	v_and_b32_e32 v31, 0xffff0000, v73
	v_lshlrev_b32_e32 v34, 16, v74
	v_and_b32_e32 v35, 0xffff0000, v74
	v_pk_add_f32 v[22:23], v[22:23], v[30:31]
	v_pk_add_f32 v[20:21], v[20:21], v[28:29]
	v_lshlrev_b32_e32 v36, 16, v75
	v_and_b32_e32 v37, 0xffff0000, v75
	v_pk_add_f32 v[30:31], v[16:17], v[34:35]
	v_mul_f32_e32 v16, v21, v21
	v_mul_f32_e32 v17, v23, v23
	v_pk_add_f32 v[28:29], v[18:19], v[36:37]
	v_fmac_f32_e32 v16, v20, v20
	v_fmac_f32_e32 v17, v22, v22
	v_add_f32_e32 v16, v16, v17
	v_mul_f32_e32 v17, v31, v31
	v_mul_f32_e32 v18, v29, v29
	v_fmac_f32_e32 v17, v30, v30
	v_fmac_f32_e32 v18, v28, v28
	v_add_f32_e32 v17, v17, v18
	v_add_f32_e32 v16, v16, v17
	v_add_f32_e32 v16, v38, v16
	v_mov_b32_e32 v17, v16
	s_nop 1
	v_permlane16_swap_b32_e32 v16, v17
	v_cvt_pk_bf16_f32 v26, v26, v27
	v_cvt_pk_bf16_f32 v27, v32, v33
	v_cvt_pk_bf16_f32 v18, v20, v21
	v_cvt_pk_bf16_f32 v19, v22, v23
	s_waitcnt lgkmcnt(0)
	v_add_f32_e32 v16, v16, v17
	v_mov_b32_e32 v17, v16
	s_nop 1
	v_permlane32_swap_b32_e32 v16, v17
	v_cvt_pk_bf16_f32 v20, v30, v31
	v_cvt_pk_bf16_f32 v21, v28, v29
	flat_store_dwordx4 v[90:91], v[24:27]
	flat_store_dwordx4 v[90:91], v[18:21] offset:256
	s_and_saveexec_b64 s[18:19], vcc
	s_cbranch_execz .LBB0_1103
	s_waitcnt lgkmcnt(0)
	v_add_f32_e32 v16, v16, v17
	v_mul_f32_e32 v16, 0x4b800000, v16
	v_trunc_f32_e32 v16, v16
	v_mul_f32_e32 v17, 0x2f800000, v16
	v_floor_f32_e32 v17, v17
	v_fmac_f32_e32 v16, 0xcf800000, v17
	v_cvt_u32_f32_e32 v16, v16
	v_cvt_u32_f32_e32 v17, v17
	v_lshl_add_u64 v[18:19], v[156:157], 3, s[8:9]
	flat_atomic_add_x2 v[18:19], v[16:17] offset:1280
.LBB0_1103:
	s_or_b64 exec, exec, s[18:19]
	v_lshlrev_b32_e32 v16, 16, v68
	s_waitcnt lgkmcnt(0)
	v_and_b32_e32 v17, 0xffff0000, v68
	v_lshlrev_b32_e32 v18, 16, v69
	v_and_b32_e32 v19, 0xffff0000, v69
	v_lshlrev_b32_e32 v20, 16, v70
	v_and_b32_e32 v21, 0xffff0000, v70
	v_lshlrev_b32_e32 v22, 16, v71
	v_and_b32_e32 v23, 0xffff0000, v71
	v_pk_add_f32 v[12:13], v[12:13], v[16:17]
	v_pk_add_f32 v[14:15], v[14:15], v[18:19]
	v_pk_add_f32 v[16:17], v[10:11], v[22:23]
	v_pk_add_f32 v[10:11], v[8:9], v[20:21]
	v_cvt_pk_bf16_f32 v8, v12, v13
	v_mul_f32_e32 v13, v13, v13
	v_fmac_f32_e32 v13, v12, v12
	v_mul_f32_e32 v12, v15, v15
	v_fmac_f32_e32 v12, v14, v14
	v_cvt_pk_bf16_f32 v9, v14, v15
	v_add_f32_e32 v12, v13, v12
	v_mul_f32_e32 v13, v11, v11
	v_mul_f32_e32 v14, v17, v17
	v_fmac_f32_e32 v13, v10, v10
	v_fmac_f32_e32 v14, v16, v16
	v_add_f32_e32 v13, v13, v14
	v_add_f32_e32 v22, v12, v13
	v_lshlrev_b32_e32 v12, 16, v64
	v_and_b32_e32 v13, 0xffff0000, v64
	v_lshlrev_b32_e32 v14, 16, v65
	v_and_b32_e32 v15, 0xffff0000, v65
	v_lshlrev_b32_e32 v18, 16, v66
	v_and_b32_e32 v19, 0xffff0000, v66
	v_pk_add_f32 v[6:7], v[6:7], v[14:15]
	v_pk_add_f32 v[4:5], v[4:5], v[12:13]
	v_lshlrev_b32_e32 v20, 16, v67
	v_and_b32_e32 v21, 0xffff0000, v67
	v_pk_add_f32 v[14:15], v[0:1], v[18:19]
	v_mul_f32_e32 v0, v5, v5
	v_mul_f32_e32 v1, v7, v7
	v_pk_add_f32 v[12:13], v[2:3], v[20:21]
	v_fmac_f32_e32 v0, v4, v4
	v_fmac_f32_e32 v1, v6, v6
	v_add_f32_e32 v0, v0, v1
	v_mul_f32_e32 v1, v15, v15
	v_mul_f32_e32 v2, v13, v13
	v_fmac_f32_e32 v1, v14, v14
	v_fmac_f32_e32 v2, v12, v12
	v_add_f32_e32 v1, v1, v2
	v_add_f32_e32 v0, v0, v1
	v_add_f32_e32 v0, v22, v0
	v_mov_b32_e32 v1, v0
	s_nop 1
	v_permlane16_swap_b32_e32 v0, v1
	v_cvt_pk_bf16_f32 v10, v10, v11
	v_cvt_pk_bf16_f32 v11, v16, v17
	v_cvt_pk_bf16_f32 v2, v4, v5
	v_cvt_pk_bf16_f32 v3, v6, v7
	s_waitcnt lgkmcnt(0)
	v_add_f32_e32 v0, v0, v1
	v_mov_b32_e32 v1, v0
	s_nop 1
	v_permlane32_swap_b32_e32 v0, v1
	v_cvt_pk_bf16_f32 v4, v14, v15
	v_cvt_pk_bf16_f32 v5, v12, v13
	flat_store_dwordx4 v[88:89], v[8:11]
	flat_store_dwordx4 v[88:89], v[2:5] offset:256
	s_and_saveexec_b64 s[18:19], vcc
	s_cbranch_execz .LBB0_1105
	s_waitcnt lgkmcnt(0)
	v_add_f32_e32 v0, v0, v1
	v_mul_f32_e32 v0, 0x4b800000, v0
	v_trunc_f32_e32 v0, v0
	v_mul_f32_e32 v1, 0x2f800000, v0
	v_floor_f32_e32 v1, v1
	v_fmac_f32_e32 v0, 0xcf800000, v1
	v_cvt_u32_f32_e32 v0, v0
	v_cvt_u32_f32_e32 v1, v1
	v_lshl_add_u64 v[2:3], v[156:157], 3, s[8:9]
	flat_atomic_add_x2 v[2:3], v[0:1] offset:1408

; __device__ __forceinline__ u64_t* ssq_ptr(unsigned char* ws, int v) { return (u64_t*)(ws + CTL_SSQ) + (size_t)v * NTOK; }
; __device__ __forceinline__ u64_t ssq_fix(float ss) { return (u64_t)(ss * 16777216.0f); }
; #define ROW_FENCE() asm volatile("" ::: "memory")
; __device__ __forceinline__ u32x4 pack8(const f32x4& a, const f32x4& b) { u32x4 w; w.x = pk_bf16(a[0], a[1]); w.y = pk_bf16(a[2], a[3]); w.z = pk_bf16(b[0], b[1]); w.w = pk_bf16(b[2], b[3]); return w; }
;     __device__ __forceinline__ void operator()(const f32x4 (&acc)[2][2][4][2], const pg8::Unit& u, int wr, int wc, int fr, int fq) const {
;         bf16_t* xb = (bf16_t*)(ws + WS_XB); u64_t* ssq = ssq_ptr(ws, v);
;         float osc = 1.0f; if constexpr (SC) osc = __uint_as_float(((const unsigned*)(ws + CTL_AMAX))[AMAX_W2]) * (1.0f / 256.0f);
;         const int col = u.pn * 256 + wc * 32 + 8 * fq;
; #pragma unroll
;         for (int ai = 0; ai < 2; ++ai) {
;             u32x4 bs[4][2];
; #pragma unroll
;             for (int m = 0; m < 4; ++m) { const size_t off = (size_t)(u.pm * 256 + ai * 128 + wr * 64 + m * 16 + fr) * D + col;
; #pragma unroll
;                 for (int bj = 0; bj < 2; ++bj) bs[m][bj] = *(const u32x4*)(xb + off + bj * 128); }
;             ROW_FENCE();
; #pragma unroll
;             for (int m = 0; m < 4; ++m) {
;                 const int row = u.pm * 256 + ai * 128 + wr * 64 + m * 16 + fr; const size_t off = (size_t)row * D + col; float ss = 0.f;
;                 float rsc = osc; if constexpr (SC) asm volatile("" : "+v"(rsc));
; #pragma unroll
;                 for (int bj = 0; bj < 2; ++bj) { f32x4 b0, b1; unpack8(bs[m][bj], b0, b1); const f32x4 x0 = SC ? b0 + acc[ai][bj][m][0] * rsc : b0 + acc[ai][bj][m][0], x1 = SC ? b1 + acc[ai][bj][m][1] * rsc : b1 + acc[ai][bj][m][1];
;                     if (!dry) *(u32x4*)(xb + off + bj * 128) = pack8(x0, x1);
;                     ss += ((x0[0] * x0[0] + x0[1] * x0[1]) + (x0[2] * x0[2] + x0[3] * x0[3])) + ((x1[0] * x1[0] + x1[1] * x1[1]) + (x1[2] * x1[2] + x1[3] * x1[3])); }
;                 ss += __shfl_xor(ss, 16); ss += __shfl_xor(ss, 32);
;                 if (fq == 0 && !dry) atomicAdd(ssq + row, ssq_fix(ss));
;             }
.LBB0_1840:
	s_mov_b32 s2, s93
	s_nop 0
	v_mbcnt_lo_u32_b32 v130, -1, s2
	v_mbcnt_hi_u32_b32 v132, -1, v130
	v_mov_b64_e32 v[130:131], s[12:13]
	flat_load_dword v130, v[130:131]
	s_lshl_b32 s2, s44, 8
	s_or_b32 s2, s2, s36
	v_cmp_gt_u32_e32 vcc, 16, v132
	s_waitcnt vmcnt(0) lgkmcnt(0)
	v_mul_f32_e32 v158, 0x3b800000, v130
	v_ashrrev_i32_e32 v130, 1, v132
	v_and_b32_e32 v130, -8, v130
	v_add_u32_e32 v130, s2, v130
	s_lshl_b32 s2, s43, 8
	s_add_i32 s2, s2, s35
	v_and_or_b32 v156, v132, 15, s2
	v_ashrrev_i32_e32 v131, 31, v130
	v_ashrrev_i32_e32 v157, 31, v156
	v_lshl_add_u64 v[160:161], v[130:131], 1, s[8:9]
	v_lshlrev_b64 v[130:131], 11, v[156:157]
	v_lshl_add_u64 v[166:167], v[160:161], 0, v[130:131]
	flat_load_dwordx4 v[172:175], v[166:167]
	flat_load_dwordx4 v[176:179], v[166:167] offset:256
	v_or_b32_e32 v130, 16, v156
	v_ashrrev_i32_e32 v131, 31, v130
	v_lshlrev_b64 v[130:131], 11, v[130:131]
	v_lshl_add_u64 v[170:171], v[160:161], 0, v[130:131]
	v_or_b32_e32 v130, 32, v156
	v_ashrrev_i32_e32 v131, 31, v130
	v_lshlrev_b64 v[130:131], 11, v[130:131]
	v_lshl_add_u64 v[168:169], v[160:161], 0, v[130:131]
	v_or_b32_e32 v130, 48, v156
	v_ashrrev_i32_e32 v131, 31, v130
	v_lshlrev_b64 v[130:131], 11, v[130:131]
	v_lshl_add_u64 v[162:163], v[160:161], 0, v[130:131]
	flat_load_dwordx4 v[150:153], v[170:171]
	flat_load_dwordx4 v[146:149], v[170:171] offset:256
	flat_load_dwordx4 v[142:145], v[168:169]
	flat_load_dwordx4 v[138:141], v[168:169] offset:256
	flat_load_dwordx4 v[134:137], v[162:163]
	flat_load_dwordx4 v[130:133], v[162:163] offset:256
	v_mov_b32_e32 v180, v158
	s_waitcnt vmcnt(0) lgkmcnt(0)
	v_lshlrev_b32_e32 v182, 16, v172
	v_and_b32_e32 v183, 0xffff0000, v172
	v_lshlrev_b32_e32 v172, 16, v173
	v_and_b32_e32 v173, 0xffff0000, v173
	v_lshlrev_b32_e32 v184, 16, v174
	v_and_b32_e32 v185, 0xffff0000, v174
	v_lshlrev_b32_e32 v174, 16, v175
	v_and_b32_e32 v175, 0xffff0000, v175
	v_pk_fma_f32 v[128:129], v[128:129], v[180:181], v[172:173] op_sel_hi:[1,0,1]
	v_pk_fma_f32 v[126:127], v[126:127], v[180:181], v[182:183] op_sel_hi:[1,0,1]
	v_pk_fma_f32 v[172:173], v[124:125], v[180:181], v[174:175] op_sel_hi:[1,0,1]
	v_pk_fma_f32 v[174:175], v[122:123], v[180:181], v[184:185] op_sel_hi:[1,0,1]
	v_cvt_pk_bf16_f32 v122, v126, v127
	v_cvt_pk_bf16_f32 v123, v128, v129
	v_cvt_pk_bf16_f32 v124, v174, v175
	v_cvt_pk_bf16_f32 v125, v172, v173
	flat_store_dwordx4 v[166:167], v[122:125]
	s_nop 1
	v_mul_f32_e32 v122, v127, v127
	v_mul_f32_e32 v123, v129, v129
	v_fmac_f32_e32 v122, v126, v126
	v_fmac_f32_e32 v123, v128, v128
	v_add_f32_e32 v122, v122, v123
	v_mul_f32_e32 v123, v175, v175
	v_mul_f32_e32 v124, v173, v173
	v_fmac_f32_e32 v123, v174, v174
	v_fmac_f32_e32 v124, v172, v172
	v_add_f32_e32 v123, v123, v124
	v_add_f32_e32 v172, v122, v123
	v_lshlrev_b32_e32 v122, 16, v176
	v_and_b32_e32 v123, 0xffff0000, v176
	v_lshlrev_b32_e32 v124, 16, v177
	v_and_b32_e32 v125, 0xffff0000, v177
	v_lshlrev_b32_e32 v126, 16, v178
	v_and_b32_e32 v127, 0xffff0000, v178
	v_lshlrev_b32_e32 v128, 16, v179
	v_and_b32_e32 v129, 0xffff0000, v179
	v_pk_fma_f32 v[120:121], v[120:121], v[180:181], v[124:125] op_sel_hi:[1,0,1]
	v_pk_fma_f32 v[118:119], v[118:119], v[180:181], v[122:123] op_sel_hi:[1,0,1]
	v_pk_fma_f32 v[122:123], v[116:117], v[180:181], v[128:129] op_sel_hi:[1,0,1]
	v_pk_fma_f32 v[124:125], v[114:115], v[180:181], v[126:127] op_sel_hi:[1,0,1]
	v_cvt_pk_bf16_f32 v114, v118, v119
	v_cvt_pk_bf16_f32 v115, v120, v121
	v_cvt_pk_bf16_f32 v116, v124, v125
	v_cvt_pk_bf16_f32 v117, v122, v123
	flat_store_dwordx4 v[166:167], v[114:117] offset:256
	s_nop 1
	v_mul_f32_e32 v114, v119, v119
	v_mul_f32_e32 v115, v121, v121
	v_fmac_f32_e32 v114, v118, v118
	v_fmac_f32_e32 v115, v120, v120
	v_add_f32_e32 v114, v114, v115
	v_mul_f32_e32 v115, v125, v125
	v_mul_f32_e32 v116, v123, v123
	v_fmac_f32_e32 v115, v124, v124
	v_fmac_f32_e32 v116, v122, v122
	v_add_f32_e32 v115, v115, v116
	v_add_f32_e32 v114, v114, v115
	v_and_b32_e32 v116, 64, v251
	v_add_f32_e32 v115, v172, v114
	v_xor_b32_e32 v114, 16, v251
	v_add_u32_e32 v117, 64, v116
	v_cmp_lt_i32_e64 s[2:3], v114, v117
	s_nop 1
	v_cndmask_b32_e64 v114, v251, v114, s[2:3]
	v_lshlrev_b32_e32 v114, 2, v114
	v_mov_b32_e32 v116, v115
	s_nop 1
	v_permlane16_swap_b32_e32 v115, v116
	s_waitcnt lgkmcnt(0)
	v_add_f32_e32 v116, v115, v116
	v_xor_b32_e32 v115, 32, v251
	v_cmp_lt_i32_e64 s[2:3], v115, v117
	s_nop 1
	v_cndmask_b32_e64 v115, v251, v115, s[2:3]
	v_lshlrev_b32_e32 v115, 2, v115
	v_mov_b32_e32 v117, v116
	s_nop 1
	v_permlane32_swap_b32_e32 v116, v117
	s_and_saveexec_b64 s[2:3], vcc
	s_cbranch_execz .LBB0_1842
	s_waitcnt lgkmcnt(0)
	v_add_f32_e32 v116, v116, v117
	v_mul_f32_e32 v116, 0x4b800000, v116
	v_trunc_f32_e32 v116, v116
	v_mul_f32_e32 v117, 0x2f800000, v116
	v_floor_f32_e32 v117, v117
	v_fmac_f32_e32 v116, 0xcf800000, v117
	v_cvt_u32_f32_e32 v116, v116
	v_cvt_u32_f32_e32 v117, v117
	v_lshl_add_u64 v[118:119], v[156:157], 3, s[10:11]
	flat_atomic_add_x2 v[118:119], v[116:117]
; __device__ __forceinline__ u64_t ssq_fix(float ss) { return (u64_t)(ss * 16777216.0f); }
; __device__ __forceinline__ u32x4 pack8(const f32x4& a, const f32x4& b) { u32x4 w; w.x = pk_bf16(a[0], a[1]); w.y = pk_bf16(a[2], a[3]); w.z = pk_bf16(b[0], b[1]); w.w = pk_bf16(b[2], b[3]); return w; }
; __device__ __forceinline__ void unpack8(const u32x4& w, f32x4& a, f32x4& b) { a = (f32x4){bf_lo(w.x), bf_hi(w.x), bf_lo(w.y), bf_hi(w.y)}; b = (f32x4){bf_lo(w.z), bf_hi(w.z), bf_lo(w.w), bf_hi(w.w)}; }
;     __device__ __forceinline__ void operator()(const f32x4 (&acc)[2][2][4][2], const pg8::Unit& u, int wr, int wc, int fr, int fq) const {
;     ...
; #pragma unroll
;             for (int m = 0; m < 4; ++m) {
;                 const int row = u.pm * 256 + ai * 128 + wr * 64 + m * 16 + fr; const size_t off = (size_t)row * D + col; float ss = 0.f;
;                 float rsc = osc; if constexpr (SC) asm volatile("" : "+v"(rsc));
; #pragma unroll
;                 for (int bj = 0; bj < 2; ++bj) { f32x4 b0, b1; unpack8(bs[m][bj], b0, b1); const f32x4 x0 = SC ? b0 + acc[ai][bj][m][0] * rsc : b0 + acc[ai][bj][m][0], x1 = SC ? b1 + acc[ai][bj][m][1] * rsc : b1 + acc[ai][bj][m][1];
;                     if (!dry) *(u32x4*)(xb + off + bj * 128) = pack8(x0, x1);
;                     ss += ((x0[0] * x0[0] + x0[1] * x0[1]) + (x0[2] * x0[2] + x0[3] * x0[3])) + ((x1[0] * x1[0] + x1[1] * x1[1]) + (x1[2] * x1[2] + x1[3] * x1[3])); }
;                 ss += __shfl_xor(ss, 16); ss += __shfl_xor(ss, 32);
;                 if (fq == 0 && !dry) atomicAdd(ssq + row, ssq_fix(ss));
;             }
.LBB0_1842:
	s_or_b64 exec, exec, s[2:3]
	v_mov_b32_e32 v116, v158
	v_lshlrev_b32_e32 v118, 16, v150
	v_and_b32_e32 v119, 0xffff0000, v150
	v_lshlrev_b32_e32 v120, 16, v151
	v_and_b32_e32 v121, 0xffff0000, v151
	v_lshlrev_b32_e32 v122, 16, v152
	v_and_b32_e32 v123, 0xffff0000, v152
	v_lshlrev_b32_e32 v124, 16, v153
	v_and_b32_e32 v125, 0xffff0000, v153
	s_waitcnt lgkmcnt(0)
	v_pk_fma_f32 v[108:109], v[108:109], v[116:117], v[118:119] op_sel_hi:[1,0,1]
	v_pk_fma_f32 v[110:111], v[110:111], v[116:117], v[120:121] op_sel_hi:[1,0,1]
	v_pk_fma_f32 v[118:119], v[106:107], v[116:117], v[124:125] op_sel_hi:[1,0,1]
	v_pk_fma_f32 v[106:107], v[104:105], v[116:117], v[122:123] op_sel_hi:[1,0,1]
	v_cvt_pk_bf16_f32 v104, v108, v109
	v_mul_f32_e32 v109, v109, v109
	v_fmac_f32_e32 v109, v108, v108
	v_mul_f32_e32 v108, v111, v111
	v_fmac_f32_e32 v108, v110, v110
	v_cvt_pk_bf16_f32 v105, v110, v111
	v_add_f32_e32 v108, v109, v108
	v_mul_f32_e32 v109, v107, v107
	v_mul_f32_e32 v110, v119, v119
	v_fmac_f32_e32 v109, v106, v106
	v_fmac_f32_e32 v110, v118, v118
	v_add_f32_e32 v109, v109, v110
	v_add_f32_e32 v117, v108, v109
	v_lshlrev_b32_e32 v108, 16, v146
	v_and_b32_e32 v109, 0xffff0000, v146
	v_lshlrev_b32_e32 v110, 16, v147
	v_and_b32_e32 v111, 0xffff0000, v147
	v_lshlrev_b32_e32 v120, 16, v148
	v_and_b32_e32 v121, 0xffff0000, v148
	v_pk_fma_f32 v[102:103], v[102:103], v[116:117], v[110:111] op_sel_hi:[1,0,1]
	v_pk_fma_f32 v[100:101], v[100:101], v[116:117], v[108:109] op_sel_hi:[1,0,1]
	v_lshlrev_b32_e32 v122, 16, v149
	v_and_b32_e32 v123, 0xffff0000, v149
	v_pk_fma_f32 v[110:111], v[96:97], v[116:117], v[120:121] op_sel_hi:[1,0,1]
	v_mul_f32_e32 v96, v101, v101
	v_mul_f32_e32 v97, v103, v103
	v_pk_fma_f32 v[108:109], v[98:99], v[116:117], v[122:123] op_sel_hi:[1,0,1]
	v_fmac_f32_e32 v96, v100, v100
	v_fmac_f32_e32 v97, v102, v102
	v_add_f32_e32 v96, v96, v97
	v_mul_f32_e32 v97, v111, v111
	v_mul_f32_e32 v98, v109, v109
	v_fmac_f32_e32 v97, v110, v110
	v_fmac_f32_e32 v98, v108, v108
	v_add_f32_e32 v97, v97, v98
	v_add_f32_e32 v96, v96, v97
	v_add_f32_e32 v96, v117, v96
	v_mov_b32_e32 v97, v96
	s_nop 1
	v_permlane16_swap_b32_e32 v96, v97
	v_cvt_pk_bf16_f32 v106, v106, v107
	v_cvt_pk_bf16_f32 v107, v118, v119
	v_cvt_pk_bf16_f32 v98, v100, v101
	v_cvt_pk_bf16_f32 v99, v102, v103
	s_waitcnt lgkmcnt(0)
	v_add_f32_e32 v96, v96, v97
	v_mov_b32_e32 v97, v96
	s_nop 1
	v_permlane32_swap_b32_e32 v96, v97
	v_cvt_pk_bf16_f32 v100, v110, v111
	v_cvt_pk_bf16_f32 v101, v108, v109
	flat_store_dwordx4 v[170:171], v[104:107]
	flat_store_dwordx4 v[170:171], v[98:101] offset:256
	s_and_saveexec_b64 s[2:3], vcc
	s_cbranch_execz .LBB0_1844
	s_waitcnt lgkmcnt(0)
	v_add_f32_e32 v96, v96, v97
	v_mul_f32_e32 v96, 0x4b800000, v96
	v_trunc_f32_e32 v96, v96
	v_mul_f32_e32 v97, 0x2f800000, v96
	v_floor_f32_e32 v97, v97
	v_fmac_f32_e32 v96, 0xcf800000, v97
	v_cvt_u32_f32_e32 v96, v96
	v_cvt_u32_f32_e32 v97, v97
	v_lshl_add_u64 v[98:99], v[156:157], 3, s[10:11]
	flat_atomic_add_x2 v[98:99], v[96:97] offset:128
.LBB0_1844:
	s_or_b64 exec, exec, s[2:3]
	v_mov_b32_e32 v96, v158
	v_lshlrev_b32_e32 v98, 16, v142
	v_and_b32_e32 v99, 0xffff0000, v142
	v_lshlrev_b32_e32 v100, 16, v143
	v_and_b32_e32 v101, 0xffff0000, v143
	v_lshlrev_b32_e32 v102, 16, v144
	v_and_b32_e32 v103, 0xffff0000, v144
	v_lshlrev_b32_e32 v104, 16, v145
	v_and_b32_e32 v105, 0xffff0000, v145
	s_waitcnt lgkmcnt(0)
	v_pk_fma_f32 v[92:93], v[92:93], v[96:97], v[98:99] op_sel_hi:[1,0,1]
	v_pk_fma_f32 v[94:95], v[94:95], v[96:97], v[100:101] op_sel_hi:[1,0,1]
	v_pk_fma_f32 v[98:99], v[90:91], v[96:97], v[104:105] op_sel_hi:[1,0,1]
	v_pk_fma_f32 v[90:91], v[88:89], v[96:97], v[102:103] op_sel_hi:[1,0,1]
	v_cvt_pk_bf16_f32 v88, v92, v93
	v_mul_f32_e32 v93, v93, v93
	v_fmac_f32_e32 v93, v92, v92
	v_mul_f32_e32 v92, v95, v95
	v_fmac_f32_e32 v92, v94, v94
	v_cvt_pk_bf16_f32 v89, v94, v95
	v_add_f32_e32 v92, v93, v92
	v_mul_f32_e32 v93, v91, v91
	v_mul_f32_e32 v94, v99, v99
	v_fmac_f32_e32 v93, v90, v90
	v_fmac_f32_e32 v94, v98, v98
	v_add_f32_e32 v93, v93, v94
	v_add_f32_e32 v97, v92, v93
	v_lshlrev_b32_e32 v92, 16, v138
	v_and_b32_e32 v93, 0xffff0000, v138
	v_lshlrev_b32_e32 v94, 16, v139
	v_and_b32_e32 v95, 0xffff0000, v139
	v_lshlrev_b32_e32 v100, 16, v140
	v_and_b32_e32 v101, 0xffff0000, v140
	v_pk_fma_f32 v[86:87], v[86:87], v[96:97], v[94:95] op_sel_hi:[1,0,1]
	v_pk_fma_f32 v[84:85], v[84:85], v[96:97], v[92:93] op_sel_hi:[1,0,1]
	v_lshlrev_b32_e32 v102, 16, v141
	v_and_b32_e32 v103, 0xffff0000, v141
	v_pk_fma_f32 v[94:95], v[80:81], v[96:97], v[100:101] op_sel_hi:[1,0,1]
	v_mul_f32_e32 v80, v85, v85
	v_mul_f32_e32 v81, v87, v87
	v_pk_fma_f32 v[92:93], v[82:83], v[96:97], v[102:103] op_sel_hi:[1,0,1]
	v_fmac_f32_e32 v80, v84, v84
	v_fmac_f32_e32 v81, v86, v86
	v_add_f32_e32 v80, v80, v81
	v_mul_f32_e32 v81, v95, v95
	v_mul_f32_e32 v82, v93, v93
	v_fmac_f32_e32 v81, v94, v94
	v_fmac_f32_e32 v82, v92, v92
	v_add_f32_e32 v81, v81, v82
	v_add_f32_e32 v80, v80, v81
	v_add_f32_e32 v80, v97, v80
	v_mov_b32_e32 v81, v80
	s_nop 1
	v_permlane16_swap_b32_e32 v80, v81
	v_cvt_pk_bf16_f32 v90, v90, v91
	v_cvt_pk_bf16_f32 v91, v98, v99
	v_cvt_pk_bf16_f32 v82, v84, v85
	v_cvt_pk_bf16_f32 v83, v86, v87
	s_waitcnt lgkmcnt(0)
	v_add_f32_e32 v80, v80, v81
	v_mov_b32_e32 v81, v80
	s_nop 1
	v_permlane32_swap_b32_e32 v80, v81
	v_cvt_pk_bf16_f32 v84, v94, v95
	v_cvt_pk_bf16_f32 v85, v92, v93
	flat_store_dwordx4 v[168:169], v[88:91]
	flat_store_dwordx4 v[168:169], v[82:85] offset:256
	s_and_saveexec_b64 s[2:3], vcc
	s_cbranch_execz .LBB0_1846
	s_waitcnt lgkmcnt(0)
	v_add_f32_e32 v80, v80, v81
	v_mul_f32_e32 v80, 0x4b800000, v80
	v_trunc_f32_e32 v80, v80
	v_mul_f32_e32 v81, 0x2f800000, v80
	v_floor_f32_e32 v81, v81
	v_fmac_f32_e32 v80, 0xcf800000, v81
	v_cvt_u32_f32_e32 v80, v80
	v_cvt_u32_f32_e32 v81, v81
	v_lshl_add_u64 v[82:83], v[156:157], 3, s[10:11]
	flat_atomic_add_x2 v[82:83], v[80:81] offset:256
; __device__ __forceinline__ u64_t ssq_fix(float ss) { return (u64_t)(ss * 16777216.0f); }
; __device__ __forceinline__ u32x4 pack8(const f32x4& a, const f32x4& b) { u32x4 w; w.x = pk_bf16(a[0], a[1]); w.y = pk_bf16(a[2], a[3]); w.z = pk_bf16(b[0], b[1]); w.w = pk_bf16(b[2], b[3]); return w; }
; __device__ __forceinline__ void unpack8(const u32x4& w, f32x4& a, f32x4& b) { a = (f32x4){bf_lo(w.x), bf_hi(w.x), bf_lo(w.y), bf_hi(w.y)}; b = (f32x4){bf_lo(w.z), bf_hi(w.z), bf_lo(w.w), bf_hi(w.w)}; }
;     __device__ __forceinline__ void operator()(const f32x4 (&acc)[2][2][4][2], const pg8::Unit& u, int wr, int wc, int fr, int fq) const {
;     ...
; #pragma unroll
;             for (int m = 0; m < 4; ++m) {
;                 const int row = u.pm * 256 + ai * 128 + wr * 64 + m * 16 + fr; const size_t off = (size_t)row * D + col; float ss = 0.f;
;                 float rsc = osc; if constexpr (SC) asm volatile("" : "+v"(rsc));
; #pragma unroll
;                 for (int bj = 0; bj < 2; ++bj) { f32x4 b0, b1; unpack8(bs[m][bj], b0, b1); const f32x4 x0 = SC ? b0 + acc[ai][bj][m][0] * rsc : b0 + acc[ai][bj][m][0], x1 = SC ? b1 + acc[ai][bj][m][1] * rsc : b1 + acc[ai][bj][m][1];
;                     if (!dry) *(u32x4*)(xb + off + bj * 128) = pack8(x0, x1);
;                     ss += ((x0[0] * x0[0] + x0[1] * x0[1]) + (x0[2] * x0[2] + x0[3] * x0[3])) + ((x1[0] * x1[0] + x1[1] * x1[1]) + (x1[2] * x1[2] + x1[3] * x1[3])); }
;                 ss += __shfl_xor(ss, 16); ss += __shfl_xor(ss, 32);
;                 if (fq == 0 && !dry) atomicAdd(ssq + row, ssq_fix(ss));
;             }
.LBB0_1846:
	s_or_b64 exec, exec, s[2:3]
	v_mov_b32_e32 v80, v158
	v_lshlrev_b32_e32 v82, 16, v134
	v_and_b32_e32 v83, 0xffff0000, v134
	v_lshlrev_b32_e32 v84, 16, v135
	v_and_b32_e32 v85, 0xffff0000, v135
	v_lshlrev_b32_e32 v86, 16, v136
	v_and_b32_e32 v87, 0xffff0000, v136
	v_lshlrev_b32_e32 v88, 16, v137
	v_and_b32_e32 v89, 0xffff0000, v137
	s_waitcnt lgkmcnt(0)
	v_pk_fma_f32 v[76:77], v[76:77], v[80:81], v[82:83] op_sel_hi:[1,0,1]
	v_pk_fma_f32 v[78:79], v[78:79], v[80:81], v[84:85] op_sel_hi:[1,0,1]
	v_pk_fma_f32 v[82:83], v[74:75], v[80:81], v[88:89] op_sel_hi:[1,0,1]
	v_pk_fma_f32 v[74:75], v[72:73], v[80:81], v[86:87] op_sel_hi:[1,0,1]
	v_cvt_pk_bf16_f32 v72, v76, v77
	v_mul_f32_e32 v77, v77, v77
	v_fmac_f32_e32 v77, v76, v76
	v_mul_f32_e32 v76, v79, v79
	v_fmac_f32_e32 v76, v78, v78
	v_cvt_pk_bf16_f32 v73, v78, v79
	v_add_f32_e32 v76, v77, v76
	v_mul_f32_e32 v77, v75, v75
	v_mul_f32_e32 v78, v83, v83
	v_fmac_f32_e32 v77, v74, v74
	v_fmac_f32_e32 v78, v82, v82
	v_add_f32_e32 v77, v77, v78
	v_add_f32_e32 v81, v76, v77
	v_lshlrev_b32_e32 v76, 16, v130
	v_and_b32_e32 v77, 0xffff0000, v130
	v_lshlrev_b32_e32 v78, 16, v131
	v_and_b32_e32 v79, 0xffff0000, v131
	v_lshlrev_b32_e32 v84, 16, v132
	v_and_b32_e32 v85, 0xffff0000, v132
	v_pk_fma_f32 v[70:71], v[70:71], v[80:81], v[78:79] op_sel_hi:[1,0,1]
	v_pk_fma_f32 v[68:69], v[68:69], v[80:81], v[76:77] op_sel_hi:[1,0,1]
	v_lshlrev_b32_e32 v86, 16, v133
	v_and_b32_e32 v87, 0xffff0000, v133
	v_pk_fma_f32 v[78:79], v[64:65], v[80:81], v[84:85] op_sel_hi:[1,0,1]
	v_mul_f32_e32 v64, v69, v69
	v_mul_f32_e32 v65, v71, v71
	v_pk_fma_f32 v[76:77], v[66:67], v[80:81], v[86:87] op_sel_hi:[1,0,1]
	v_fmac_f32_e32 v64, v68, v68
	v_fmac_f32_e32 v65, v70, v70
	v_add_f32_e32 v64, v64, v65
	v_mul_f32_e32 v65, v79, v79
	v_mul_f32_e32 v66, v77, v77
	v_fmac_f32_e32 v65, v78, v78
	v_fmac_f32_e32 v66, v76, v76
	v_add_f32_e32 v65, v65, v66
	v_add_f32_e32 v64, v64, v65
	v_add_f32_e32 v64, v81, v64
	v_mov_b32_e32 v65, v64
	s_nop 1
	v_permlane16_swap_b32_e32 v64, v65
	v_cvt_pk_bf16_f32 v74, v74, v75
	v_cvt_pk_bf16_f32 v75, v82, v83
	v_cvt_pk_bf16_f32 v66, v68, v69
	v_cvt_pk_bf16_f32 v67, v70, v71
	s_waitcnt lgkmcnt(0)
	v_add_f32_e32 v64, v64, v65
	v_mov_b32_e32 v65, v64
	s_nop 1
	v_permlane32_swap_b32_e32 v64, v65
	v_cvt_pk_bf16_f32 v68, v78, v79
	v_cvt_pk_bf16_f32 v69, v76, v77
	flat_store_dwordx4 v[162:163], v[72:75]
	flat_store_dwordx4 v[162:163], v[66:69] offset:256
	s_and_saveexec_b64 s[2:3], vcc
	s_cbranch_execz .LBB0_1848
	s_waitcnt lgkmcnt(0)
	v_add_f32_e32 v64, v64, v65
	v_mul_f32_e32 v64, 0x4b800000, v64
	v_trunc_f32_e32 v64, v64
	v_mul_f32_e32 v65, 0x2f800000, v64
	v_floor_f32_e32 v65, v65
	v_fmac_f32_e32 v64, 0xcf800000, v65
	v_cvt_u32_f32_e32 v64, v64
	v_cvt_u32_f32_e32 v65, v65
	v_lshl_add_u64 v[66:67], v[156:157], 3, s[10:11]
	flat_atomic_add_x2 v[66:67], v[64:65] offset:384
.LBB0_1848:
	s_or_b64 exec, exec, s[2:3]
	v_add_u32_e32 v64, 0x80, v156
	s_waitcnt lgkmcnt(0)
	v_ashrrev_i32_e32 v65, 31, v64
	v_lshlrev_b64 v[64:65], 11, v[64:65]
	v_lshl_add_u64 v[98:99], v[160:161], 0, v[64:65]
	flat_load_dwordx4 v[100:103], v[98:99]
	flat_load_dwordx4 v[88:91], v[98:99] offset:256
	v_add_u32_e32 v64, 0x90, v156
	v_ashrrev_i32_e32 v65, 31, v64
	v_lshlrev_b64 v[64:65], 11, v[64:65]
	v_lshl_add_u64 v[96:97], v[160:161], 0, v[64:65]
	v_add_u32_e32 v64, 0xa0, v156
	v_ashrrev_i32_e32 v65, 31, v64
	v_lshlrev_b64 v[64:65], 11, v[64:65]
	v_lshl_add_u64 v[94:95], v[160:161], 0, v[64:65]
	v_add_u32_e32 v64, 0xb0, v156
	v_ashrrev_i32_e32 v65, 31, v64
	v_lshlrev_b64 v[64:65], 11, v[64:65]
	v_lshl_add_u64 v[92:93], v[160:161], 0, v[64:65]
	flat_load_dwordx4 v[84:87], v[96:97]
	flat_load_dwordx4 v[80:83], v[96:97] offset:256
	flat_load_dwordx4 v[76:79], v[94:95]
	flat_load_dwordx4 v[72:75], v[94:95] offset:256
	flat_load_dwordx4 v[68:71], v[92:93]
	flat_load_dwordx4 v[64:67], v[92:93] offset:256
	v_mov_b32_e32 v104, v158
	s_waitcnt vmcnt(0) lgkmcnt(0)
	v_lshlrev_b32_e32 v106, 16, v100
	v_and_b32_e32 v107, 0xffff0000, v100
	v_lshlrev_b32_e32 v100, 16, v101
	v_and_b32_e32 v101, 0xffff0000, v101
	v_lshlrev_b32_e32 v108, 16, v102
	v_and_b32_e32 v109, 0xffff0000, v102
	v_lshlrev_b32_e32 v102, 16, v103
	v_and_b32_e32 v103, 0xffff0000, v103
	v_pk_fma_f32 v[62:63], v[62:63], v[104:105], v[100:101] op_sel_hi:[1,0,1]
	v_pk_fma_f32 v[60:61], v[60:61], v[104:105], v[106:107] op_sel_hi:[1,0,1]
	v_pk_fma_f32 v[100:101], v[58:59], v[104:105], v[102:103] op_sel_hi:[1,0,1]
	v_pk_fma_f32 v[102:103], v[56:57], v[104:105], v[108:109] op_sel_hi:[1,0,1]
	v_cvt_pk_bf16_f32 v56, v60, v61
	v_cvt_pk_bf16_f32 v57, v62, v63
	v_cvt_pk_bf16_f32 v58, v102, v103
	v_cvt_pk_bf16_f32 v59, v100, v101
	flat_store_dwordx4 v[98:99], v[56:59]
	s_nop 1
	v_mul_f32_e32 v56, v61, v61
	v_mul_f32_e32 v57, v63, v63
	v_fmac_f32_e32 v56, v60, v60
	v_fmac_f32_e32 v57, v62, v62
	v_add_f32_e32 v56, v56, v57
	v_mul_f32_e32 v57, v103, v103
	v_mul_f32_e32 v58, v101, v101
	v_fmac_f32_e32 v57, v102, v102
	v_fmac_f32_e32 v58, v100, v100
	v_add_f32_e32 v57, v57, v58
	v_add_f32_e32 v100, v56, v57
	v_lshlrev_b32_e32 v56, 16, v88
	v_and_b32_e32 v57, 0xffff0000, v88
	v_lshlrev_b32_e32 v58, 16, v89
	v_and_b32_e32 v59, 0xffff0000, v89
	v_lshlrev_b32_e32 v60, 16, v90
	v_and_b32_e32 v61, 0xffff0000, v90
	v_lshlrev_b32_e32 v62, 16, v91
	v_and_b32_e32 v63, 0xffff0000, v91
	v_pk_fma_f32 v[54:55], v[54:55], v[104:105], v[58:59] op_sel_hi:[1,0,1]
	v_pk_fma_f32 v[52:53], v[52:53], v[104:105], v[56:57] op_sel_hi:[1,0,1]
	v_pk_fma_f32 v[56:57], v[50:51], v[104:105], v[62:63] op_sel_hi:[1,0,1]
	v_pk_fma_f32 v[58:59], v[48:49], v[104:105], v[60:61] op_sel_hi:[1,0,1]
	v_cvt_pk_bf16_f32 v48, v52, v53
	v_cvt_pk_bf16_f32 v49, v54, v55
	v_cvt_pk_bf16_f32 v50, v58, v59
	v_cvt_pk_bf16_f32 v51, v56, v57
	flat_store_dwordx4 v[98:99], v[48:51] offset:256
	s_nop 1
	v_mul_f32_e32 v48, v53, v53
	v_mul_f32_e32 v49, v55, v55
	v_fmac_f32_e32 v48, v52, v52
	v_fmac_f32_e32 v49, v54, v54
	v_add_f32_e32 v48, v48, v49
	v_mul_f32_e32 v49, v59, v59
	v_mul_f32_e32 v50, v57, v57
	v_fmac_f32_e32 v49, v58, v58
	v_fmac_f32_e32 v50, v56, v56
	v_add_f32_e32 v49, v49, v50
	v_add_f32_e32 v48, v48, v49
	v_add_f32_e32 v48, v100, v48
	v_mov_b32_e32 v49, v48
	s_nop 1
	v_permlane16_swap_b32_e32 v48, v49
	s_waitcnt lgkmcnt(0)
	v_add_f32_e32 v48, v48, v49
	v_mov_b32_e32 v49, v48
	s_nop 1
	v_permlane32_swap_b32_e32 v48, v49
	s_and_saveexec_b64 s[2:3], vcc
	s_cbranch_execz .LBB0_1850
	s_waitcnt lgkmcnt(0)
	v_add_f32_e32 v48, v48, v49
	v_mul_f32_e32 v48, 0x4b800000, v48
	v_trunc_f32_e32 v48, v48
	v_mul_f32_e32 v49, 0x2f800000, v48
	v_floor_f32_e32 v49, v49
	v_fmac_f32_e32 v48, 0xcf800000, v49
	v_cvt_u32_f32_e32 v48, v48
	v_cvt_u32_f32_e32 v49, v49
	v_lshl_add_u64 v[50:51], v[156:157], 3, s[10:11]
	flat_atomic_add_x2 v[50:51], v[48:49] offset:1024
; __device__ __forceinline__ u64_t ssq_fix(float ss) { return (u64_t)(ss * 16777216.0f); }
; __device__ __forceinline__ u32x4 pack8(const f32x4& a, const f32x4& b) { u32x4 w; w.x = pk_bf16(a[0], a[1]); w.y = pk_bf16(a[2], a[3]); w.z = pk_bf16(b[0], b[1]); w.w = pk_bf16(b[2], b[3]); return w; }
; __device__ __forceinline__ void unpack8(const u32x4& w, f32x4& a, f32x4& b) { a = (f32x4){bf_lo(w.x), bf_hi(w.x), bf_lo(w.y), bf_hi(w.y)}; b = (f32x4){bf_lo(w.z), bf_hi(w.z), bf_lo(w.w), bf_hi(w.w)}; }
;     __device__ __forceinline__ void operator()(const f32x4 (&acc)[2][2][4][2], const pg8::Unit& u, int wr, int wc, int fr, int fq) const {
;     ...
; #pragma unroll
;             for (int m = 0; m < 4; ++m) {
;                 const int row = u.pm * 256 + ai * 128 + wr * 64 + m * 16 + fr; const size_t off = (size_t)row * D + col; float ss = 0.f;
;                 float rsc = osc; if constexpr (SC) asm volatile("" : "+v"(rsc));
; #pragma unroll
;                 for (int bj = 0; bj < 2; ++bj) { f32x4 b0, b1; unpack8(bs[m][bj], b0, b1); const f32x4 x0 = SC ? b0 + acc[ai][bj][m][0] * rsc : b0 + acc[ai][bj][m][0], x1 = SC ? b1 + acc[ai][bj][m][1] * rsc : b1 + acc[ai][bj][m][1];
;                     if (!dry) *(u32x4*)(xb + off + bj * 128) = pack8(x0, x1);
;                     ss += ((x0[0] * x0[0] + x0[1] * x0[1]) + (x0[2] * x0[2] + x0[3] * x0[3])) + ((x1[0] * x1[0] + x1[1] * x1[1]) + (x1[2] * x1[2] + x1[3] * x1[3])); }
;                 ss += __shfl_xor(ss, 16); ss += __shfl_xor(ss, 32);
;                 if (fq == 0 && !dry) atomicAdd(ssq + row, ssq_fix(ss));
;             }
.LBB0_1850:
	s_or_b64 exec, exec, s[2:3]
	v_mov_b32_e32 v48, v158
	v_lshlrev_b32_e32 v50, 16, v84
	v_and_b32_e32 v51, 0xffff0000, v84
	v_lshlrev_b32_e32 v52, 16, v85
	v_and_b32_e32 v53, 0xffff0000, v85
	v_lshlrev_b32_e32 v54, 16, v86
	v_and_b32_e32 v55, 0xffff0000, v86
	v_lshlrev_b32_e32 v56, 16, v87
	v_and_b32_e32 v57, 0xffff0000, v87
	s_waitcnt lgkmcnt(0)
	v_pk_fma_f32 v[44:45], v[44:45], v[48:49], v[50:51] op_sel_hi:[1,0,1]
	v_pk_fma_f32 v[46:47], v[46:47], v[48:49], v[52:53] op_sel_hi:[1,0,1]
	v_pk_fma_f32 v[50:51], v[42:43], v[48:49], v[56:57] op_sel_hi:[1,0,1]
	v_pk_fma_f32 v[42:43], v[40:41], v[48:49], v[54:55] op_sel_hi:[1,0,1]
	v_cvt_pk_bf16_f32 v40, v44, v45
	v_mul_f32_e32 v45, v45, v45
	v_fmac_f32_e32 v45, v44, v44
	v_mul_f32_e32 v44, v47, v47
	v_fmac_f32_e32 v44, v46, v46
	v_cvt_pk_bf16_f32 v41, v46, v47
	v_add_f32_e32 v44, v45, v44
	v_mul_f32_e32 v45, v43, v43
	v_mul_f32_e32 v46, v51, v51
	v_fmac_f32_e32 v45, v42, v42
	v_fmac_f32_e32 v46, v50, v50
	v_add_f32_e32 v45, v45, v46
	v_add_f32_e32 v49, v44, v45
	v_lshlrev_b32_e32 v44, 16, v80
	v_and_b32_e32 v45, 0xffff0000, v80
	v_lshlrev_b32_e32 v46, 16, v81
	v_and_b32_e32 v47, 0xffff0000, v81
	v_lshlrev_b32_e32 v52, 16, v82
	v_and_b32_e32 v53, 0xffff0000, v82
	v_pk_fma_f32 v[38:39], v[38:39], v[48:49], v[46:47] op_sel_hi:[1,0,1]
	v_pk_fma_f32 v[36:37], v[36:37], v[48:49], v[44:45] op_sel_hi:[1,0,1]
	v_lshlrev_b32_e32 v54, 16, v83
	v_and_b32_e32 v55, 0xffff0000, v83
	v_pk_fma_f32 v[46:47], v[32:33], v[48:49], v[52:53] op_sel_hi:[1,0,1]
	v_mul_f32_e32 v32, v37, v37
	v_mul_f32_e32 v33, v39, v39
	v_pk_fma_f32 v[44:45], v[34:35], v[48:49], v[54:55] op_sel_hi:[1,0,1]
	v_fmac_f32_e32 v32, v36, v36
	v_fmac_f32_e32 v33, v38, v38
	v_add_f32_e32 v32, v32, v33
	v_mul_f32_e32 v33, v47, v47
	v_mul_f32_e32 v34, v45, v45
	v_fmac_f32_e32 v33, v46, v46
	v_fmac_f32_e32 v34, v44, v44
	v_add_f32_e32 v33, v33, v34
	v_add_f32_e32 v32, v32, v33
	v_add_f32_e32 v32, v49, v32
	v_mov_b32_e32 v33, v32
	s_nop 1
	v_permlane16_swap_b32_e32 v32, v33
	v_cvt_pk_bf16_f32 v42, v42, v43
	v_cvt_pk_bf16_f32 v43, v50, v51
	v_cvt_pk_bf16_f32 v34, v36, v37
	v_cvt_pk_bf16_f32 v35, v38, v39
	s_waitcnt lgkmcnt(0)
	v_add_f32_e32 v32, v32, v33
	v_mov_b32_e32 v33, v32
	s_nop 1
	v_permlane32_swap_b32_e32 v32, v33
	v_cvt_pk_bf16_f32 v36, v46, v47
	v_cvt_pk_bf16_f32 v37, v44, v45
	flat_store_dwordx4 v[96:97], v[40:43]
	flat_store_dwordx4 v[96:97], v[34:37] offset:256
	s_and_saveexec_b64 s[2:3], vcc
	s_cbranch_execz .LBB0_1852
	s_waitcnt lgkmcnt(0)
	v_add_f32_e32 v32, v32, v33
	v_mul_f32_e32 v32, 0x4b800000, v32
	v_trunc_f32_e32 v32, v32
	v_mul_f32_e32 v33, 0x2f800000, v32
	v_floor_f32_e32 v33, v33
	v_fmac_f32_e32 v32, 0xcf800000, v33
	v_cvt_u32_f32_e32 v32, v32
	v_cvt_u32_f32_e32 v33, v33
	v_lshl_add_u64 v[34:35], v[156:157], 3, s[10:11]
	flat_atomic_add_x2 v[34:35], v[32:33] offset:1152
; __device__ __forceinline__ u64_t ssq_fix(float ss) { return (u64_t)(ss * 16777216.0f); }
; __device__ __forceinline__ u32x4 pack8(const f32x4& a, const f32x4& b) { u32x4 w; w.x = pk_bf16(a[0], a[1]); w.y = pk_bf16(a[2], a[3]); w.z = pk_bf16(b[0], b[1]); w.w = pk_bf16(b[2], b[3]); return w; }
; __device__ __forceinline__ void unpack8(const u32x4& w, f32x4& a, f32x4& b) { a = (f32x4){bf_lo(w.x), bf_hi(w.x), bf_lo(w.y), bf_hi(w.y)}; b = (f32x4){bf_lo(w.z), bf_hi(w.z), bf_lo(w.w), bf_hi(w.w)}; }
;     __device__ __forceinline__ void operator()(const f32x4 (&acc)[2][2][4][2], const pg8::Unit& u, int wr, int wc, int fr, int fq) const {
;     ...
; #pragma unroll
;             for (int m = 0; m < 4; ++m) {
;                 const int row = u.pm * 256 + ai * 128 + wr * 64 + m * 16 + fr; const size_t off = (size_t)row * D + col; float ss = 0.f;
;                 float rsc = osc; if constexpr (SC) asm volatile("" : "+v"(rsc));
; #pragma unroll
;                 for (int bj = 0; bj < 2; ++bj) { f32x4 b0, b1; unpack8(bs[m][bj], b0, b1); const f32x4 x0 = SC ? b0 + acc[ai][bj][m][0] * rsc : b0 + acc[ai][bj][m][0], x1 = SC ? b1 + acc[ai][bj][m][1] * rsc : b1 + acc[ai][bj][m][1];
;                     if (!dry) *(u32x4*)(xb + off + bj * 128) = pack8(x0, x1);
;                     ss += ((x0[0] * x0[0] + x0[1] * x0[1]) + (x0[2] * x0[2] + x0[3] * x0[3])) + ((x1[0] * x1[0] + x1[1] * x1[1]) + (x1[2] * x1[2] + x1[3] * x1[3])); }
;                 ss += __shfl_xor(ss, 16); ss += __shfl_xor(ss, 32);
;                 if (fq == 0 && !dry) atomicAdd(ssq + row, ssq_fix(ss));
;             }
.LBB0_1852:
	s_or_b64 exec, exec, s[2:3]
	v_mov_b32_e32 v32, v158
	v_lshlrev_b32_e32 v34, 16, v76
	v_and_b32_e32 v35, 0xffff0000, v76
	v_lshlrev_b32_e32 v36, 16, v77
	v_and_b32_e32 v37, 0xffff0000, v77
	v_lshlrev_b32_e32 v38, 16, v78
	v_and_b32_e32 v39, 0xffff0000, v78
	v_lshlrev_b32_e32 v40, 16, v79
	v_and_b32_e32 v41, 0xffff0000, v79
	s_waitcnt lgkmcnt(0)
	v_pk_fma_f32 v[28:29], v[28:29], v[32:33], v[34:35] op_sel_hi:[1,0,1]
	v_pk_fma_f32 v[30:31], v[30:31], v[32:33], v[36:37] op_sel_hi:[1,0,1]
	v_pk_fma_f32 v[34:35], v[26:27], v[32:33], v[40:41] op_sel_hi:[1,0,1]
	v_pk_fma_f32 v[26:27], v[24:25], v[32:33], v[38:39] op_sel_hi:[1,0,1]
	v_cvt_pk_bf16_f32 v24, v28, v29
	v_mul_f32_e32 v29, v29, v29
	v_fmac_f32_e32 v29, v28, v28
	v_mul_f32_e32 v28, v31, v31
	v_fmac_f32_e32 v28, v30, v30
	v_cvt_pk_bf16_f32 v25, v30, v31
	v_add_f32_e32 v28, v29, v28
	v_mul_f32_e32 v29, v27, v27
	v_mul_f32_e32 v30, v35, v35
	v_fmac_f32_e32 v29, v26, v26
	v_fmac_f32_e32 v30, v34, v34
	v_add_f32_e32 v29, v29, v30
	v_add_f32_e32 v33, v28, v29
	v_lshlrev_b32_e32 v28, 16, v72
	v_and_b32_e32 v29, 0xffff0000, v72
	v_lshlrev_b32_e32 v30, 16, v73
	v_and_b32_e32 v31, 0xffff0000, v73
	v_lshlrev_b32_e32 v36, 16, v74
	v_and_b32_e32 v37, 0xffff0000, v74
	v_pk_fma_f32 v[22:23], v[22:23], v[32:33], v[30:31] op_sel_hi:[1,0,1]
	v_pk_fma_f32 v[20:21], v[20:21], v[32:33], v[28:29] op_sel_hi:[1,0,1]
	v_lshlrev_b32_e32 v38, 16, v75
	v_and_b32_e32 v39, 0xffff0000, v75
	v_pk_fma_f32 v[30:31], v[16:17], v[32:33], v[36:37] op_sel_hi:[1,0,1]
	v_mul_f32_e32 v16, v21, v21
	v_mul_f32_e32 v17, v23, v23
	v_pk_fma_f32 v[28:29], v[18:19], v[32:33], v[38:39] op_sel_hi:[1,0,1]
	v_fmac_f32_e32 v16, v20, v20
	v_fmac_f32_e32 v17, v22, v22
	v_add_f32_e32 v16, v16, v17
	v_mul_f32_e32 v17, v31, v31
	v_mul_f32_e32 v18, v29, v29
	v_fmac_f32_e32 v17, v30, v30
	v_fmac_f32_e32 v18, v28, v28
	v_add_f32_e32 v17, v17, v18
	v_add_f32_e32 v16, v16, v17
	v_add_f32_e32 v16, v33, v16
	v_mov_b32_e32 v17, v16
	s_nop 1
	v_permlane16_swap_b32_e32 v16, v17
	v_cvt_pk_bf16_f32 v26, v26, v27
	v_cvt_pk_bf16_f32 v27, v34, v35
	v_cvt_pk_bf16_f32 v18, v20, v21
	v_cvt_pk_bf16_f32 v19, v22, v23
	s_waitcnt lgkmcnt(0)
	v_add_f32_e32 v16, v16, v17
	v_mov_b32_e32 v17, v16
	s_nop 1
	v_permlane32_swap_b32_e32 v16, v17
	v_cvt_pk_bf16_f32 v20, v30, v31
	v_cvt_pk_bf16_f32 v21, v28, v29
	flat_store_dwordx4 v[94:95], v[24:27]
	flat_store_dwordx4 v[94:95], v[18:21] offset:256
	s_and_saveexec_b64 s[2:3], vcc
	s_cbranch_execz .LBB0_1854
	s_waitcnt lgkmcnt(0)
	v_add_f32_e32 v16, v16, v17
	v_mul_f32_e32 v16, 0x4b800000, v16
	v_trunc_f32_e32 v16, v16
	v_mul_f32_e32 v17, 0x2f800000, v16
	v_floor_f32_e32 v17, v17
	v_fmac_f32_e32 v16, 0xcf800000, v17
	v_cvt_u32_f32_e32 v16, v16
	v_cvt_u32_f32_e32 v17, v17
	v_lshl_add_u64 v[18:19], v[156:157], 3, s[10:11]
	flat_atomic_add_x2 v[18:19], v[16:17] offset:1280
.LBB0_1854:
	s_or_b64 exec, exec, s[2:3]
	v_lshlrev_b32_e32 v16, 16, v68
	s_waitcnt lgkmcnt(0)
	v_and_b32_e32 v17, 0xffff0000, v68
	v_lshlrev_b32_e32 v18, 16, v69
	v_and_b32_e32 v19, 0xffff0000, v69
	v_lshlrev_b32_e32 v20, 16, v70
	v_and_b32_e32 v21, 0xffff0000, v70
	v_lshlrev_b32_e32 v22, 16, v71
	v_and_b32_e32 v23, 0xffff0000, v71
	v_pk_fma_f32 v[12:13], v[12:13], v[158:159], v[16:17] op_sel_hi:[1,0,1]
	v_pk_fma_f32 v[14:15], v[14:15], v[158:159], v[18:19] op_sel_hi:[1,0,1]
	v_pk_fma_f32 v[16:17], v[10:11], v[158:159], v[22:23] op_sel_hi:[1,0,1]
	v_pk_fma_f32 v[10:11], v[8:9], v[158:159], v[20:21] op_sel_hi:[1,0,1]
	v_cvt_pk_bf16_f32 v8, v12, v13
	v_mul_f32_e32 v13, v13, v13
	v_fmac_f32_e32 v13, v12, v12
	v_mul_f32_e32 v12, v15, v15
	v_fmac_f32_e32 v12, v14, v14
	v_cvt_pk_bf16_f32 v9, v14, v15
	v_add_f32_e32 v12, v13, v12
	v_mul_f32_e32 v13, v11, v11
	v_mul_f32_e32 v14, v17, v17
	v_fmac_f32_e32 v13, v10, v10
	v_fmac_f32_e32 v14, v16, v16
	v_add_f32_e32 v13, v13, v14
	v_add_f32_e32 v22, v12, v13
	v_lshlrev_b32_e32 v12, 16, v64
	v_and_b32_e32 v13, 0xffff0000, v64
	v_lshlrev_b32_e32 v14, 16, v65
	v_and_b32_e32 v15, 0xffff0000, v65
	v_lshlrev_b32_e32 v18, 16, v66
	v_and_b32_e32 v19, 0xffff0000, v66
	v_pk_fma_f32 v[6:7], v[6:7], v[158:159], v[14:15] op_sel_hi:[1,0,1]
	v_pk_fma_f32 v[4:5], v[4:5], v[158:159], v[12:13] op_sel_hi:[1,0,1]
	v_lshlrev_b32_e32 v20, 16, v67
	v_and_b32_e32 v21, 0xffff0000, v67
	v_pk_fma_f32 v[14:15], v[0:1], v[158:159], v[18:19] op_sel_hi:[1,0,1]
	v_mul_f32_e32 v0, v5, v5
	v_mul_f32_e32 v1, v7, v7
	v_pk_fma_f32 v[12:13], v[2:3], v[158:159], v[20:21] op_sel_hi:[1,0,1]
	v_fmac_f32_e32 v0, v4, v4
	v_fmac_f32_e32 v1, v6, v6
	v_add_f32_e32 v0, v0, v1
	v_mul_f32_e32 v1, v15, v15
	v_mul_f32_e32 v2, v13, v13
	v_fmac_f32_e32 v1, v14, v14
	v_fmac_f32_e32 v2, v12, v12
	v_add_f32_e32 v1, v1, v2
	v_add_f32_e32 v0, v0, v1
	v_add_f32_e32 v0, v22, v0
	v_mov_b32_e32 v1, v0
	s_nop 1
	v_permlane16_swap_b32_e32 v0, v1
	v_cvt_pk_bf16_f32 v10, v10, v11
	v_cvt_pk_bf16_f32 v11, v16, v17
	v_cvt_pk_bf16_f32 v2, v4, v5
	v_cvt_pk_bf16_f32 v3, v6, v7
	s_waitcnt lgkmcnt(0)
	v_add_f32_e32 v0, v0, v1
	v_mov_b32_e32 v1, v0
	s_nop 1
	v_permlane32_swap_b32_e32 v0, v1
	v_cvt_pk_bf16_f32 v4, v14, v15
	v_cvt_pk_bf16_f32 v5, v12, v13
	flat_store_dwordx4 v[92:93], v[8:11]
	flat_store_dwordx4 v[92:93], v[2:5] offset:256
	s_and_saveexec_b64 s[2:3], vcc
	s_cbranch_execz .LBB0_1856
	s_waitcnt lgkmcnt(0)
	v_add_f32_e32 v0, v0, v1
	v_mul_f32_e32 v0, 0x4b800000, v0
	v_trunc_f32_e32 v0, v0
	v_mul_f32_e32 v1, 0x2f800000, v0
	v_floor_f32_e32 v1, v1
	v_fmac_f32_e32 v0, 0xcf800000, v1
	v_cvt_u32_f32_e32 v0, v0
	v_cvt_u32_f32_e32 v1, v1
	v_lshl_add_u64 v[2:3], v[156:157], 3, s[10:11]
	flat_atomic_add_x2 v[2:3], v[0:1] offset:1408
